# stack: P4b in-register scan state, P0 x->fp8 loop contiguous 8-wide, P4a tile-X loads issued right after the unit inputs land, P5 prefetch wait moved to the latch
# baseline (speedup 1.0000x reference)
; #define GAS __attribute__((address_space(1)))
; __device__ __forceinline__ void p0_prologue(Frame& F0, const In& I) {
;     ...
;     for (size_t i = gt; i < (size_t)T * D / 8; i += NGT) { const f32x4 a = ((const GAS f32x4*)I.x)[2 * i], b = ((const GAS f32x4*)I.x)[2 * i + 1];
;         int w0 = __builtin_amdgcn_cvt_pk_fp8_f32(a.x, a.y, 0, false); w0 = __builtin_amdgcn_cvt_pk_fp8_f32(a.z, a.w, w0, true);
;         int w1 = __builtin_amdgcn_cvt_pk_fp8_f32(b.x, b.y, 0, false); w1 = __builtin_amdgcn_cvt_pk_fp8_f32(b.z, b.w, w1, true);
;         ((GAS v2u*)(ws + WS_XB8))[i] = (v2u){(unsigned)w0, (unsigned)w1}; }
.LBB0_58:
	s_or_b64 exec, exec, s[2:3]
	s_mov_b32 s0, 0x800000
	v_cmp_gt_u32_e32 vcc, s0, v6
	s_and_saveexec_b64 s[0:1], vcc
	s_cbranch_execz .LBB0_61
	v_mov_b32_e32 v7, 0
	v_readlane_b32 s16, v254, 5
	v_lshlrev_b64 v[4:5], 5, v[6:7]
	v_readlane_b32 s17, v254, 6
	s_ashr_i32 s13, s12, 31
	v_lshl_add_u64 v[2:3], v[6:7], 3, s[96:97]
	s_mov_b64 s[2:3], 0xe8000000
	v_lshl_add_u64 v[4:5], s[16:17], 0, v[4:5]
	v_lshl_add_u64 v[2:3], v[2:3], 0, s[2:3]
	s_lshl_b64 s[2:3], s[12:13], 3
	v_lshl_add_u64 v[4:5], v[4:5], 0, 16
	s_lshl_b64 s[4:5], s[12:13], 5
	s_mov_b64 s[6:7], 0
	s_mov_b64 s[8:9], 0x7fffff
	v_readlane_b32 s18, v254, 7
	v_readlane_b32 s19, v254, 8
	v_readlane_b32 s20, v254, 9
	v_readlane_b32 s21, v254, 10
	v_readlane_b32 s22, v254, 11
	v_readlane_b32 s23, v254, 12
	v_readlane_b32 s24, v254, 13
	v_readlane_b32 s25, v254, 14
	v_readlane_b32 s26, v254, 15
	v_readlane_b32 s27, v254, 16
	v_readlane_b32 s28, v254, 17
	v_readlane_b32 s29, v254, 18
	v_readlane_b32 s30, v254, 19
	v_readlane_b32 s31, v254, 20
	s_lshl_b64 s[100:101], s[12:13], 3
	s_sub_u32 s98, s100, s12
	s_subb_u32 s99, s101, s13
	v_mbcnt_lo_u32_b32 v104, -1, 0
	v_mbcnt_hi_u32_b32 v104, -1, v104
	v_lshlrev_b32_e32 v105, 4, v104
	v_add_u32_e32 v105, 16, v105
	v_mov_b32_e32 v106, 0
	v_sub_co_u32_e32 v108, vcc, v4, v105
	s_nop 1
	v_subb_co_u32_e32 v109, vcc, v5, v106, vcc
	v_lshlrev_b32_e32 v105, 2, v104
	v_sub_co_u32_e32 v110, vcc, v2, v105
	s_nop 1
	v_subb_co_u32_e32 v111, vcc, v3, v106, vcc
.Lx8_head:
	v_cmp_lt_u64_e32 vcc, s[8:9], v[6:7]
	s_nop 1
	s_andn2_b64 exec, exec, vcc
	s_cbranch_execz .LBB0_61
	s_cmp_eq_u64 exec, -1
	s_cbranch_scc0 .LBB0_60
	v_lshl_add_u64 v[18:19], v[6:7], 0, s[98:99]
	v_cmp_lt_u64_e32 vcc, s[8:9], v[18:19]
	s_cbranch_vccnz .LBB0_60
	v_mov_b64_e32 v[100:101], v[108:109]
	v_mov_b64_e32 v[102:103], v[110:111]
	global_load_dwordx4 v[20:23], v[100:101], off
	global_load_dwordx4 v[24:27], v[100:101], off offset:1024
	v_lshl_add_u64 v[100:101], v[100:101], 0, s[4:5]
	global_load_dwordx4 v[28:31], v[100:101], off
	global_load_dwordx4 v[32:35], v[100:101], off offset:1024
	v_lshl_add_u64 v[100:101], v[100:101], 0, s[4:5]
	global_load_dwordx4 v[36:39], v[100:101], off
	global_load_dwordx4 v[40:43], v[100:101], off offset:1024
	v_lshl_add_u64 v[100:101], v[100:101], 0, s[4:5]
	global_load_dwordx4 v[44:47], v[100:101], off
	global_load_dwordx4 v[48:51], v[100:101], off offset:1024
	v_lshl_add_u64 v[100:101], v[100:101], 0, s[4:5]
	global_load_dwordx4 v[52:55], v[100:101], off
	global_load_dwordx4 v[56:59], v[100:101], off offset:1024
	v_lshl_add_u64 v[100:101], v[100:101], 0, s[4:5]
	global_load_dwordx4 v[60:63], v[100:101], off
	global_load_dwordx4 v[64:67], v[100:101], off offset:1024
	v_lshl_add_u64 v[100:101], v[100:101], 0, s[4:5]
	global_load_dwordx4 v[68:71], v[100:101], off
	global_load_dwordx4 v[72:75], v[100:101], off offset:1024
	v_lshl_add_u64 v[100:101], v[100:101], 0, s[4:5]
	global_load_dwordx4 v[76:79], v[100:101], off
	global_load_dwordx4 v[80:83], v[100:101], off offset:1024
	v_lshl_add_u64 v[6:7], v[6:7], 0, s[100:101]
	s_lshl_b64 vcc, s[100:101], 5
	v_lshl_add_u64 v[4:5], v[4:5], 0, vcc
	v_lshl_add_u64 v[108:109], v[108:109], 0, vcc
	v_lshl_add_u64 v[2:3], s[100:101], 3, v[2:3]
	v_lshl_add_u64 v[110:111], s[100:101], 3, v[110:111]
	s_waitcnt vmcnt(14)
	v_mov_b32_e32 v84, 0
	v_mov_b32_e32 v85, 0
	v_cvt_pk_fp8_f32 v84, v20, v21
	v_cvt_pk_fp8_f32 v85, v24, v25
	v_cvt_pk_fp8_f32 v84, v22, v23 op_sel:[0,0,1]
	v_cvt_pk_fp8_f32 v85, v26, v27 op_sel:[0,0,1]
	global_store_dword v[102:103], v84, off
	global_store_dword v[102:103], v85, off offset:256
	v_lshl_add_u64 v[102:103], v[102:103], 0, s[2:3]
	s_waitcnt vmcnt(14)
	v_mov_b32_e32 v86, 0
	v_mov_b32_e32 v87, 0
	v_cvt_pk_fp8_f32 v86, v28, v29
	v_cvt_pk_fp8_f32 v87, v32, v33
	v_cvt_pk_fp8_f32 v86, v30, v31 op_sel:[0,0,1]
	v_cvt_pk_fp8_f32 v87, v34, v35 op_sel:[0,0,1]
	global_store_dword v[102:103], v86, off
	global_store_dword v[102:103], v87, off offset:256
	v_lshl_add_u64 v[102:103], v[102:103], 0, s[2:3]
	s_waitcnt vmcnt(14)
	v_mov_b32_e32 v88, 0
	v_mov_b32_e32 v89, 0
	v_cvt_pk_fp8_f32 v88, v36, v37
	v_cvt_pk_fp8_f32 v89, v40, v41
	v_cvt_pk_fp8_f32 v88, v38, v39 op_sel:[0,0,1]
	v_cvt_pk_fp8_f32 v89, v42, v43 op_sel:[0,0,1]
	global_store_dword v[102:103], v88, off
	global_store_dword v[102:103], v89, off offset:256
	v_lshl_add_u64 v[102:103], v[102:103], 0, s[2:3]
	s_waitcnt vmcnt(14)
	v_mov_b32_e32 v90, 0
	v_mov_b32_e32 v91, 0
	v_cvt_pk_fp8_f32 v90, v44, v45
	v_cvt_pk_fp8_f32 v91, v48, v49
	v_cvt_pk_fp8_f32 v90, v46, v47 op_sel:[0,0,1]
	v_cvt_pk_fp8_f32 v91, v50, v51 op_sel:[0,0,1]
	global_store_dword v[102:103], v90, off
	global_store_dword v[102:103], v91, off offset:256
	v_lshl_add_u64 v[102:103], v[102:103], 0, s[2:3]
	s_waitcnt vmcnt(14)
	v_mov_b32_e32 v92, 0
	v_mov_b32_e32 v93, 0
	v_cvt_pk_fp8_f32 v92, v52, v53
	v_cvt_pk_fp8_f32 v93, v56, v57
	v_cvt_pk_fp8_f32 v92, v54, v55 op_sel:[0,0,1]
	v_cvt_pk_fp8_f32 v93, v58, v59 op_sel:[0,0,1]
	global_store_dword v[102:103], v92, off
	global_store_dword v[102:103], v93, off offset:256
	v_lshl_add_u64 v[102:103], v[102:103], 0, s[2:3]
	s_waitcnt vmcnt(14)
	v_mov_b32_e32 v94, 0
	v_mov_b32_e32 v95, 0
	v_cvt_pk_fp8_f32 v94, v60, v61
	v_cvt_pk_fp8_f32 v95, v64, v65
	v_cvt_pk_fp8_f32 v94, v62, v63 op_sel:[0,0,1]
	v_cvt_pk_fp8_f32 v95, v66, v67 op_sel:[0,0,1]
	global_store_dword v[102:103], v94, off
	global_store_dword v[102:103], v95, off offset:256
	v_lshl_add_u64 v[102:103], v[102:103], 0, s[2:3]
	s_waitcnt vmcnt(14)
	v_mov_b32_e32 v96, 0
	v_mov_b32_e32 v97, 0
	v_cvt_pk_fp8_f32 v96, v68, v69
	v_cvt_pk_fp8_f32 v97, v72, v73
	v_cvt_pk_fp8_f32 v96, v70, v71 op_sel:[0,0,1]
	v_cvt_pk_fp8_f32 v97, v74, v75 op_sel:[0,0,1]
	global_store_dword v[102:103], v96, off
	global_store_dword v[102:103], v97, off offset:256
	v_lshl_add_u64 v[102:103], v[102:103], 0, s[2:3]
	s_waitcnt vmcnt(14)
	v_mov_b32_e32 v98, 0
	v_mov_b32_e32 v99, 0
	v_cvt_pk_fp8_f32 v98, v76, v77
	v_cvt_pk_fp8_f32 v99, v80, v81
	v_cvt_pk_fp8_f32 v98, v78, v79 op_sel:[0,0,1]
	v_cvt_pk_fp8_f32 v99, v82, v83 op_sel:[0,0,1]
	global_store_dword v[102:103], v98, off
	global_store_dword v[102:103], v99, off offset:256
	s_branch .Lx8_head

; #define LAS __attribute__((address_space(3)))
; __device__ __forceinline__ void p4a_chunk(Frame& F0, const In& I) {
;     ...
;         for (int j = 0; j < 8; ++j) { const float sg = ((const LAS float*)(L + C_SEG))[j * 64 + lane]; tot += sg; pre += (j < w) ? sg : 0.f; }
;         if (w == 0) ((LAS float*)(L + C_GAM))[lane] = __expf(tot);
;         unsigned att[4], bht[4], kht[4], vtt[4];
;         float at_[8], bh_[8], kh_[8]; const float gtot = __expf(tot); float ep_prev = 1.f;
; #pragma unroll
;         for (int i = 0; i < 8; ++i) { const int t = 8 * w + i; const float cum = pre + cs[i], cump = cum - lwv[i];
;             const float kkv = kk[i] * kkp; const float n2 = wave_sum(kkv * kkv); const float kkn = kkv * __builtin_amdgcn_rsqf(fmaxf(n2, 1e-24f));
;             const float a = -kkn, bb = kkn * ic[i], kp = kk[i] * (1.0f + (ic[i] - 1.0f) * kap);
;             const float ep = __expf(cum), em = __builtin_amdgcn_rcpf(ep), epp = (i == 0) ? __expf(cump) : ep_prev, eL = gtot * em; ep_prev = ep;
;             const float Rv = rr[i] * ep, Av = a * epp, Bv = bb * em, Kv = kp * em;
;             at_[i] = Av; bh_[i] = bb * eL; kh_[i] = kp * eL;
.LBB0_1085:
	v_readlane_b32 s14, v255, 14
	v_readlane_b32 s15, v255, 15
	v_lshlrev_b32_e32 v189, 16, v90
	v_lshlrev_b32_e32 v109, 16, v97
	v_cndmask_b32_e64 v82, 0, v82, s[14:15]
	v_readlane_b32 s14, v255, 16
	v_readlane_b32 s15, v255, 17
	s_waitcnt vmcnt(5)
	v_lshlrev_b32_e32 v97, 16, v186
	v_add_u32_e32 v194, s90, v120
	v_cndmask_b32_e64 v83, 0, v83, s[14:15]
	v_readlane_b32 s14, v255, 18
	v_readlane_b32 s15, v255, 19
	v_add_f32_e32 v82, v82, v83
	v_lshlrev_b32_e32 v104, 16, v95
	v_cndmask_b32_e64 v83, 0, v86, s[14:15]
	v_readlane_b32 s14, v255, 20
	v_readlane_b32 s15, v255, 21
	v_add_f32_e32 v82, v82, v83
	v_lshlrev_b32_e32 v95, 16, v96
	v_cndmask_b32_e64 v83, 0, v87, s[14:15]
	v_readlane_b32 s14, v255, 22
	v_readlane_b32 s15, v255, 23
	v_add_f32_e32 v82, v82, v83
	v_lshlrev_b32_e32 v190, 16, v99
	v_cndmask_b32_e64 v83, 0, v92, s[14:15]
	v_readlane_b32 s14, v255, 24
	v_readlane_b32 s15, v255, 25
	v_add_f32_e32 v82, v82, v83
	v_lshlrev_b32_e32 v96, 16, v113
	v_cndmask_b32_e64 v83, 0, v93, s[14:15]
	v_readlane_b32 s14, v255, 26
	v_readlane_b32 s15, v255, 27
	v_add_f32_e32 v82, v82, v83
	v_lshlrev_b32_e32 v113, 16, v114
	v_cndmask_b32_e64 v83, 0, v100, s[14:15]
	v_readlane_b32 s14, v255, 28
	v_readlane_b32 s15, v255, 29
	v_add_f32_e32 v82, v82, v83
	v_lshlrev_b32_e32 v105, 16, v102
	v_cndmask_b32_e64 v83, 0, v101, s[14:15]
	v_add_f32_e32 v193, v82, v83
	v_add_f32_e32 v83, v187, v193
	v_mul_f32_e32 v82, 0x3fb8aa3b, v83
	v_exp_f32_e32 v82, v82
	v_sub_f32_e32 v83, v83, v89
	v_mul_f32_e32 v83, 0x3fb8aa3b, v83
	v_exp_f32_e32 v186, v83
	v_mul_f32_e32 v83, v82, v189
	v_bfe_u32 v89, v83, 16, 1
	v_add3_u32 v83, v83, v89, s3
	v_add_f32_e32 v89, v185, v193
	v_mul_f32_e32 v89, 0x3fb8aa3b, v89
	v_exp_f32_e32 v187, v89
	ds_write_b16_d16_hi v194, v83
	v_add_f32_e32 v83, v184, v193
	v_mul_f32_e32 v83, 0x3fb8aa3b, v83
	v_mul_f32_e32 v89, v187, v95
	v_exp_f32_e32 v83, v83
	v_bfe_u32 v95, v89, 16, 1
	v_add3_u32 v89, v89, v95, s3
	v_add_f32_e32 v95, v183, v193
	v_mul_f32_e32 v95, 0x3fb8aa3b, v95
	v_exp_f32_e32 v114, v95
	ds_write_b16_d16_hi v194, v89 offset:144
	v_mul_f32_e32 v89, v83, v190
	v_add_f32_e32 v100, v181, v193
	v_bfe_u32 v95, v89, 16, 1
	v_mul_f32_e32 v100, 0x3fb8aa3b, v100
	v_lshlrev_b32_e32 v102, 16, v106
	v_lshlrev_b32_e32 v80, 16, v85
	v_lshlrev_b32_e32 v85, 16, v103
	v_lshlrev_b32_e32 v103, 16, v112
	v_add3_u32 v89, v89, v95, s3
	v_exp_f32_e32 v112, v100
	ds_write_b16_d16_hi v194, v89 offset:288
	v_mul_f32_e32 v89, v114, v102
	v_add_f32_e32 v101, v180, v193
	v_bfe_u32 v95, v89, 16, 1
	v_mul_f32_e32 v101, 0x3fb8aa3b, v101
	v_lshlrev_b32_e32 v108, 16, v84
	v_lshlrev_b32_e32 v84, 16, v91
	v_lshlrev_b32_e32 v91, 16, v115
	v_add3_u32 v89, v89, v95, s3
	v_exp_f32_e32 v115, v101
	ds_write_b16_d16_hi v194, v89 offset:432
	v_mul_f32_e32 v89, v112, v103
	v_bfe_u32 v95, v89, 16, 1
	v_add3_u32 v89, v89, v95, s3
	v_add_f32_e32 v95, v179, v193
	ds_write_b16_d16_hi v194, v89 offset:576
	v_mul_f32_e32 v89, v115, v113
	v_mul_f32_e32 v95, 0x3fb8aa3b, v95
	v_exp_f32_e32 v113, v95
	v_bfe_u32 v95, v89, 16, 1
	v_add3_u32 v89, v89, v95, s3
	v_add_f32_e32 v95, v178, v193
	v_mul_f32_e32 v95, 0x3fb8aa3b, v95
	v_lshlrev_b32_e32 v191, 16, v177
	v_exp_f32_e32 v95, v95
	ds_write_b16_d16_hi v194, v89 offset:720
	v_mul_f32_e32 v89, v113, v191
	v_bfe_u32 v103, v89, 16, 1
	s_waitcnt vmcnt(4)
	v_lshlrev_b32_e32 v192, 16, v188
	v_add3_u32 v89, v89, v103, s3
	v_lshlrev_b32_e32 v81, 16, v98
	ds_write_b16_d16_hi v194, v89 offset:864
	v_mul_f32_e32 v89, v95, v192
	s_waitcnt vmcnt(1)
	v_pk_mul_f32 v[178:179], v[88:89], v[80:81] op_sel_hi:[0,1]
	v_pk_mul_f32 v[180:181], v[178:179], v[178:179]
	v_rcp_f32_e32 v103, v95
	v_lshlrev_b32_e32 v93, 16, v182
	v_add_f32_dpp v95, v180, v180 quad_perm:[1,0,3,2] row_mask:0xf bank_mask:0xf bound_ctrl:1
	v_rcp_f32_e32 v182, v187
	v_lshlrev_b32_e32 v99, 16, v176
	v_add_f32_dpp v95, v95, v95 quad_perm:[2,3,0,1] row_mask:0xf bank_mask:0xf bound_ctrl:1
	v_rcp_f32_e32 v176, v82
	v_rcp_f32_e32 v177, v83
	v_add_f32_dpp v95, v95, v95 row_ror:4 row_mask:0xf bank_mask:0xf bound_ctrl:1
	v_pk_add_f32 v[86:87], v[108:109], -1.0 op_sel_hi:[1,0]
	v_pk_add_f32 v[188:189], v[104:105], -1.0 op_sel_hi:[1,0]
	v_add_f32_dpp v95, v95, v95 row_ror:8 row_mask:0xf bank_mask:0xf bound_ctrl:1
	v_rcp_f32_e32 v183, v114
	v_readlane_b32 s16, v95, 16
	v_readlane_b32 s17, v95, 48
	v_readlane_b32 s14, v95, 0
	v_readlane_b32 s15, v95, 32
	v_mov_b32_e32 v184, s16
	v_mov_b32_e32 v185, s17
	v_pk_add_f32 v[184:185], s[14:15], v[184:185]
	v_lshlrev_b32_e32 v90, 16, v107
	v_add_f32_e32 v95, v184, v185
	v_max_f32_e32 v95, 0x179abe15, v95
	v_rsq_f32_e32 v180, v95
	v_rcp_f32_e32 v102, v115
	v_add_f32_dpp v95, v181, v181 quad_perm:[1,0,3,2] row_mask:0xf bank_mask:0xf bound_ctrl:1
	v_lshlrev_b32_e32 v92, 16, v111
	v_lshlrev_b32_e32 v98, 16, v110
	v_add_f32_dpp v95, v95, v95 quad_perm:[2,3,0,1] row_mask:0xf bank_mask:0xf bound_ctrl:1
	v_rcp_f32_e32 v100, v112
	v_pk_add_f32 v[106:107], v[98:99], -1.0 op_sel_hi:[1,0]
	v_add_f32_dpp v95, v95, v95 row_ror:4 row_mask:0xf bank_mask:0xf bound_ctrl:1
	v_rcp_f32_e32 v101, v113
	v_pk_add_f32 v[110:111], v[96:97], -1.0 op_sel_hi:[1,0]
	v_add_f32_dpp v95, v95, v95 row_ror:8 row_mask:0xf bank_mask:0xf bound_ctrl:1
	s_cmp_lt_i32 s85, 0x18000
	v_readlane_b32 s16, v95, 16
	v_readlane_b32 s17, v95, 48
	v_readlane_b32 s14, v95, 0
	v_readlane_b32 s15, v95, 32
	v_mov_b32_e32 v184, s16
	v_mov_b32_e32 v185, s17
	v_pk_add_f32 v[184:185], s[14:15], v[184:185]
	s_cselect_b64 s[74:75], -1, 0
	v_add_f32_e32 v95, v184, v185
	v_max_f32_e32 v95, 0x179abe15, v95
	v_rsq_f32_e32 v181, v95
	v_bfe_u32 v95, v89, 16, 1
	v_add3_u32 v89, v89, v95, s3
	ds_write_b16_d16_hi v194, v89 offset:1008
; __device__ __forceinline__ void tr8_load(const MoeItem& m, f32x4 (&v)[16], int lane) {
;     const int kr = lane >> 4, cq = lane & 15;
;     const int voff = (kr * m.ldw + 4 * cq) * 4;
; #pragma unroll
;     for (int i = 0; i < 16; ++i) v[i] = __builtin_bit_cast(f32x4, __builtin_amdgcn_raw_buffer_load_b128(m.rs, voff, (int)(m.soff + (unsigned)i * m.rstep), 0));
; }
; __device__ __forceinline__ MoeItem moe_item(int r, const float* w_gu, const float* w_down, unsigned char* ws) {
;     MoeItem m;
;     if (r < MOE_J4) { const int e = r / 2048, q = r % 2048, kb = q / 64, cb = q % 64, c0 = cb * 64; const int cc = c0 & 2047;
;         m.rs = __builtin_amdgcn_make_buffer_rsrc((void*)w_gu, 0, 0xffffffff, 0x00020000); m.ldw = 2 * FF; m.k0 = kb * 64;
;         m.soff = (unsigned)(((size_t)e * D * 2 * FF + (size_t)kb * 64 * (2 * FF) + c0) * 4); m.rstep = 4u * (2 * FF) * 4u;
;         m.WT = ws + WS_WGUT + (size_t)e * 2 * FF * D; m.ldt = D; m.drow = (cc >> 7) * 256 + (c0 >= 2048 ? 128 : 0) + (cc & 127); }
;     else { r -= MOE_J4; const int e = r / 1024, q = r % 1024, kb = q / 32, cb = q % 32;
;         m.rs = __builtin_amdgcn_make_buffer_rsrc((void*)w_down, 0, 0xffffffff, 0x00020000); m.ldw = D; m.k0 = kb * 64;
;         m.soff = (unsigned)(((size_t)e * FF * D + (size_t)kb * 64 * D + cb * 64) * 4); m.rstep = 4u * D * 4u;
;         m.WT = ws + WS_WDNT + (size_t)e * D * FF; m.ldt = FF; m.drow = cb * 64; }
;     return m;
	v_pk_mul_f32 v[178:179], v[178:179], v[180:181]
	s_mov_b64 s[64:65], -1
	v_pk_mul_f32 v[180:181], v[186:187], v[178:179] neg_lo:[0,1] neg_hi:[0,1]
	v_pk_mul_f32 v[108:109], v[178:179], v[108:109]
	v_and_b32_sdwa v89, v181, v159 dst_sel:DWORD dst_unused:UNUSED_PAD src0_sel:WORD_1 src1_sel:DWORD
	v_and_b32_sdwa v95, v180, v159 dst_sel:DWORD dst_unused:UNUSED_PAD src0_sel:WORD_1 src1_sel:DWORD
	v_add3_u32 v89, v181, v89, s3
	v_add3_u32 v95, v180, v95, s3
	v_pk_mul_f32 v[180:181], v[88:89], v[84:85] op_sel_hi:[0,1]
	v_pk_mul_f32 v[184:185], v[180:181], v[180:181]
	ds_write_b16_d16_hi v194, v95 offset:55296
	s_nop 0
	v_add_f32_dpp v184, v184, v184 quad_perm:[1,0,3,2] row_mask:0xf bank_mask:0xf bound_ctrl:1
	v_add_f32_dpp v185, v185, v185 quad_perm:[1,0,3,2] row_mask:0xf bank_mask:0xf bound_ctrl:1
	s_nop 0
	v_add_f32_dpp v184, v184, v184 quad_perm:[2,3,0,1] row_mask:0xf bank_mask:0xf bound_ctrl:1
	v_add_f32_dpp v185, v185, v185 quad_perm:[2,3,0,1] row_mask:0xf bank_mask:0xf bound_ctrl:1
	s_nop 0
	v_add_f32_dpp v184, v184, v184 row_ror:4 row_mask:0xf bank_mask:0xf bound_ctrl:1
	v_add_f32_dpp v185, v185, v185 row_ror:4 row_mask:0xf bank_mask:0xf bound_ctrl:1
	s_nop 0
	v_add_f32_dpp v184, v184, v184 row_ror:8 row_mask:0xf bank_mask:0xf bound_ctrl:1
	v_add_f32_dpp v185, v185, v185 row_ror:8 row_mask:0xf bank_mask:0xf bound_ctrl:1
	v_readlane_b32 s16, v184, 16
	v_readlane_b32 s17, v184, 48
	v_readlane_b32 s14, v184, 0
	v_readlane_b32 s15, v184, 32
	v_mov_b32_e32 v186, s16
	v_mov_b32_e32 v187, s17
	v_pk_add_f32 v[186:187], s[14:15], v[186:187]
	v_readlane_b32 s16, v185, 16
	v_readlane_b32 s17, v185, 48
	v_add_f32_e32 v184, v186, v187
	v_readlane_b32 s14, v185, 0
	v_readlane_b32 s15, v185, 32
	v_mov_b32_e32 v186, s16
	v_mov_b32_e32 v187, s17
	v_pk_add_f32 v[186:187], s[14:15], v[186:187]
	v_max_f32_e32 v184, 0x179abe15, v184
	v_add_f32_e32 v185, v186, v187
	v_max_f32_e32 v185, 0x179abe15, v185
	v_rsq_f32_e32 v184, v184
	v_rsq_f32_e32 v185, v185
	v_lshrrev_b32_e32 v186, 16, v95
	v_lshrrev_b32_e32 v187, 16, v89
	v_pk_mul_f32 v[180:181], v[180:181], v[184:185]
	s_nop 0
	v_pk_mul_f32 v[82:83], v[82:83], v[180:181] neg_lo:[0,1] neg_hi:[0,1]
	v_pk_mul_f32 v[104:105], v[180:181], v[104:105]
	v_and_b32_sdwa v95, v83, v159 dst_sel:DWORD dst_unused:UNUSED_PAD src0_sel:WORD_1 src1_sel:DWORD
	v_and_b32_sdwa v184, v82, v159 dst_sel:DWORD dst_unused:UNUSED_PAD src0_sel:WORD_1 src1_sel:DWORD
	v_add3_u32 v185, v83, v95, s3
	v_add3_u32 v184, v82, v184, s3
	s_waitcnt vmcnt(0)
	s_cmp_lt_i32 s85, 0x18000
	s_cselect_b32 s48, s85, 0
	s_cmp_gt_i32 s48, 0xffff
	s_cbranch_scc1 .Lxh_down
	s_lshr_b32 s49, s48, 11
	s_lshl_b32 s49, s49, 25
	s_bfe_u32 s54, s48, 0x50006
	s_lshl_b32 s54, s54, 20
	s_add_i32 s49, s49, s54
	s_and_b32 s54, s48, 63
	s_lshl_b32 s54, s54, 8
	s_add_i32 s49, s49, s54
	s_mov_b32 s55, 0x10000
	s_movk_i32 s56, 0x4000
	v_readlane_b32 s60, v255, 54
	v_readlane_b32 s61, v255, 55
	s_branch .Lxh_go
.Lxh_down:
	s_add_i32 s48, s48, 0xffff0000
	s_lshr_b32 s49, s48, 10
	s_lshl_b32 s49, s49, 24
	s_bfe_u32 s54, s48, 0x50005
	s_lshl_b32 s54, s54, 19
	s_add_i32 s49, s49, s54
	s_and_b32 s54, s48, 31
	s_lshl_b32 s54, s54, 8
	s_add_i32 s49, s49, s54
	s_mov_b32 s55, 0x8000
	s_movk_i32 s56, 0x2000
	v_readlane_b32 s60, v255, 52
	v_readlane_b32 s61, v255, 53
.Lxh_go:
	s_mov_b32 s62, -1
	s_mov_b32 s63, 0x20000
	v_mul_u32_u24_e32 v62, s56, v116
	v_lshl_or_b32 v62, v128, 2, v62
	s_nop 4
	buffer_load_dwordx4 v[2:5], v62, s[60:63], s49 offen
	s_add_i32 s49, s49, s55
	buffer_load_dwordx4 v[6:9], v62, s[60:63], s49 offen
	s_add_i32 s49, s49, s55
	buffer_load_dwordx4 v[10:13], v62, s[60:63], s49 offen
	s_add_i32 s49, s49, s55
	buffer_load_dwordx4 v[14:17], v62, s[60:63], s49 offen
	s_add_i32 s49, s49, s55
	buffer_load_dwordx4 v[18:21], v62, s[60:63], s49 offen
	s_add_i32 s49, s49, s55
	buffer_load_dwordx4 v[22:25], v62, s[60:63], s49 offen
	s_add_i32 s49, s49, s55
	buffer_load_dwordx4 v[26:29], v62, s[60:63], s49 offen
	s_add_i32 s49, s49, s55
	buffer_load_dwordx4 v[30:33], v62, s[60:63], s49 offen
	s_add_i32 s49, s49, s55
	buffer_load_dwordx4 v[34:37], v62, s[60:63], s49 offen
	s_add_i32 s49, s49, s55
	buffer_load_dwordx4 v[38:41], v62, s[60:63], s49 offen
	s_add_i32 s49, s49, s55
	buffer_load_dwordx4 v[42:45], v62, s[60:63], s49 offen
	s_add_i32 s49, s49, s55
	buffer_load_dwordx4 v[46:49], v62, s[60:63], s49 offen
	s_add_i32 s49, s49, s55
	buffer_load_dwordx4 v[50:53], v62, s[60:63], s49 offen
	s_add_i32 s49, s49, s55
	buffer_load_dwordx4 v[54:57], v62, s[60:63], s49 offen
	s_add_i32 s49, s49, s55
	buffer_load_dwordx4 v[58:61], v62, s[60:63], s49 offen
	s_add_i32 s49, s49, s55
	buffer_load_dwordx4 v[62:65], v62, s[60:63], s49 offen
	v_pk_fma_f32 v[82:83], v[86:87], v[68:69], 1.0 op_sel_hi:[1,0,0]
	ds_write_b16_d16_hi v194, v184 offset:55440
	ds_write_b16_d16_hi v194, v89 offset:55584
	ds_write_b16_d16_hi v194, v185 offset:55728
	v_pk_mul_f32 v[80:81], v[82:83], v[80:81]
	v_pk_mul_f32 v[82:83], v[94:95], v[176:177] op_sel_hi:[0,1]
	v_mul_f32_e32 v86, v80, v176
	v_bfe_u32 v87, v86, 16, 1
	v_add3_u32 v86, v86, v87, s3
	ds_write_b16_d16_hi v71, v86
	v_pk_fma_f32 v[86:87], v[188:189], v[68:69], 1.0 op_sel_hi:[1,0,0]
	s_nop 0
	v_pk_mul_f32 v[84:85], v[86:87], v[84:85]
	v_pk_mul_f32 v[86:87], v[94:95], v[182:183] op_sel_hi:[0,1]
	v_mul_f32_e32 v89, v84, v182
	v_bfe_u32 v95, v89, 16, 1
	v_add3_u32 v89, v89, v95, s3
	ds_write_b16_d16_hi v71, v89 offset:144
	v_mul_f32_e32 v89, v81, v177
	v_bfe_u32 v95, v89, 16, 1
	v_add3_u32 v89, v89, v95, s3
	ds_write_b16_d16_hi v71, v89 offset:288
	v_mul_f32_e32 v89, v85, v183
	v_bfe_u32 v95, v89, 16, 1
	v_add3_u32 v89, v89, v95, s3
	ds_write_b16_d16_hi v71, v89 offset:432
; #define LAS __attribute__((address_space(3)))
; __device__ __forceinline__ unsigned f2bf(float f) { unsigned u = __builtin_bit_cast(unsigned, f); return (u + 0x7fffu + ((u >> 16) & 1u)) >> 16; }
; __device__ __forceinline__ void p4a_chunk(Frame& F0, const In& I) {
;     ...
;         for (int i = 0; i < 8; ++i) { const int t = 8 * w + i; const float cum = pre + cs[i], cump = cum - lwv[i];
;             const float kkv = kk[i] * kkp; const float n2 = wave_sum(kkv * kkv); const float kkn = kkv * __builtin_amdgcn_rsqf(fmaxf(n2, 1e-24f));
;             const float a = -kkn, bb = kkn * ic[i], kp = kk[i] * (1.0f + (ic[i] - 1.0f) * kap);
;             const float ep = __expf(cum), em = __builtin_amdgcn_rcpf(ep), epp = (i == 0) ? __expf(cump) : ep_prev, eL = gtot * em; ep_prev = ep;
;             const float Rv = rr[i] * ep, Av = a * epp, Bv = bb * em, Kv = kp * em;
;             at_[i] = Av; bh_[i] = bb * eL; kh_[i] = kp * eL;
;             *(LAS unsigned short*)(L + C_RT + t * CP + lane * 2) = (unsigned short)f2bf(Rv);
;             *(LAS unsigned short*)(L + C_AT + t * CP + lane * 2) = (unsigned short)f2bf(Av);
;             *(LAS unsigned short*)(L + C_BT + t * CP + lane * 2) = (unsigned short)f2bf(Bv);
;             *(LAS unsigned short*)(L + C_KT + t * CP + lane * 2) = (unsigned short)f2bf(Kv); }
	v_mul_f32_e32 v89, v176, v108
	v_bfe_u32 v95, v89, 16, 1
	v_add3_u32 v89, v89, v95, s3
	ds_write_b16_d16_hi v194, v89 offset:64512
	v_mul_f32_e32 v89, v182, v104
	v_bfe_u32 v95, v89, 16, 1
	v_add3_u32 v89, v89, v95, s3
	ds_write_b16_d16_hi v194, v89 offset:64656
	v_mul_f32_e32 v89, v177, v109
	v_bfe_u32 v95, v89, 16, 1
	v_add3_u32 v89, v89, v95, s3
	ds_write_b16_d16_hi v194, v89 offset:64800
	v_mul_f32_e32 v89, v183, v105
	v_bfe_u32 v95, v89, 16, 1
	v_add3_u32 v89, v89, v95, s3
	v_pk_mul_f32 v[176:177], v[88:89], v[90:91] op_sel_hi:[0,1]
	v_pk_mul_f32 v[178:179], v[176:177], v[176:177]
	ds_write_b16_d16_hi v194, v89 offset:64944
	v_pk_mul_f32 v[104:105], v[86:87], v[104:105]
	v_add_f32_dpp v95, v178, v178 quad_perm:[1,0,3,2] row_mask:0xf bank_mask:0xf bound_ctrl:1
	v_pk_mul_f32 v[108:109], v[82:83], v[108:109]
	s_nop 0
	v_add_f32_dpp v95, v95, v95 quad_perm:[2,3,0,1] row_mask:0xf bank_mask:0xf bound_ctrl:1
	s_nop 1
	v_add_f32_dpp v95, v95, v95 row_ror:4 row_mask:0xf bank_mask:0xf bound_ctrl:1
	s_nop 1
	v_add_f32_dpp v95, v95, v95 row_ror:8 row_mask:0xf bank_mask:0xf bound_ctrl:1
	s_nop 0
	v_readlane_b32 s16, v95, 16
	v_readlane_b32 s17, v95, 48
	v_readlane_b32 s14, v95, 0
	v_readlane_b32 s15, v95, 32
	v_mov_b32_e32 v180, s16
	v_mov_b32_e32 v181, s17
	v_pk_add_f32 v[180:181], s[14:15], v[180:181]
	s_nop 0
	v_add_f32_e32 v95, v180, v181
	v_max_f32_e32 v95, 0x179abe15, v95
	v_rsq_f32_e32 v178, v95
	s_nop 0
	v_add_f32_dpp v95, v179, v179 quad_perm:[1,0,3,2] row_mask:0xf bank_mask:0xf bound_ctrl:1
	s_nop 1
	v_add_f32_dpp v95, v95, v95 quad_perm:[2,3,0,1] row_mask:0xf bank_mask:0xf bound_ctrl:1
	s_nop 1
	v_add_f32_dpp v95, v95, v95 row_ror:4 row_mask:0xf bank_mask:0xf bound_ctrl:1
	s_nop 1
	v_add_f32_dpp v95, v95, v95 row_ror:8 row_mask:0xf bank_mask:0xf bound_ctrl:1
	s_nop 0
	v_readlane_b32 s16, v95, 16
	v_readlane_b32 s17, v95, 48
	v_readlane_b32 s14, v95, 0
	v_readlane_b32 s15, v95, 32
	v_mov_b32_e32 v180, s16
	v_mov_b32_e32 v181, s17
	v_pk_add_f32 v[180:181], s[14:15], v[180:181]
	s_nop 0
	v_add_f32_e32 v95, v180, v181
	v_max_f32_e32 v95, 0x179abe15, v95
	v_rsq_f32_e32 v179, v95
	s_nop 0
	v_pk_mul_f32 v[176:177], v[176:177], v[178:179]
	s_nop 0
	v_pk_mul_f32 v[114:115], v[114:115], v[176:177] neg_lo:[0,1] neg_hi:[0,1]
	v_pk_mul_f32 v[98:99], v[176:177], v[98:99]
	v_and_b32_sdwa v89, v115, v159 dst_sel:DWORD dst_unused:UNUSED_PAD src0_sel:WORD_1 src1_sel:DWORD
	v_and_b32_sdwa v95, v114, v159 dst_sel:DWORD dst_unused:UNUSED_PAD src0_sel:WORD_1 src1_sel:DWORD
	v_add3_u32 v180, v115, v89, s3
	v_pk_mul_f32 v[88:89], v[88:89], v[92:93] op_sel_hi:[0,1]
	v_add3_u32 v95, v114, v95, s3
	v_pk_mul_f32 v[114:115], v[88:89], v[88:89]
	ds_write_b16_d16_hi v194, v95 offset:55872
	s_nop 0
	v_add_f32_dpp v114, v114, v114 quad_perm:[1,0,3,2] row_mask:0xf bank_mask:0xf bound_ctrl:1
	v_add_f32_dpp v115, v115, v115 quad_perm:[1,0,3,2] row_mask:0xf bank_mask:0xf bound_ctrl:1
	s_nop 0
	v_add_f32_dpp v114, v114, v114 quad_perm:[2,3,0,1] row_mask:0xf bank_mask:0xf bound_ctrl:1
	v_add_f32_dpp v115, v115, v115 quad_perm:[2,3,0,1] row_mask:0xf bank_mask:0xf bound_ctrl:1
	s_nop 0
	v_add_f32_dpp v114, v114, v114 row_ror:4 row_mask:0xf bank_mask:0xf bound_ctrl:1
	v_add_f32_dpp v115, v115, v115 row_ror:4 row_mask:0xf bank_mask:0xf bound_ctrl:1
	s_nop 0
	v_add_f32_dpp v114, v114, v114 row_ror:8 row_mask:0xf bank_mask:0xf bound_ctrl:1
	v_add_f32_dpp v115, v115, v115 row_ror:8 row_mask:0xf bank_mask:0xf bound_ctrl:1
	v_readlane_b32 s16, v114, 16
	v_readlane_b32 s17, v114, 48
	v_readlane_b32 s14, v114, 0
	v_readlane_b32 s15, v114, 32
	v_mov_b32_e32 v178, s16
	v_mov_b32_e32 v179, s17
	v_pk_add_f32 v[178:179], s[14:15], v[178:179]
	v_readlane_b32 s16, v115, 16
	v_readlane_b32 s17, v115, 48
	v_add_f32_e32 v114, v178, v179
	v_readlane_b32 s14, v115, 0
	v_readlane_b32 s15, v115, 32
; #define LAS __attribute__((address_space(3)))
; __device__ __forceinline__ unsigned f2bf(float f) { unsigned u = __builtin_bit_cast(unsigned, f); return (u + 0x7fffu + ((u >> 16) & 1u)) >> 16; }
; __device__ __forceinline__ unsigned pk2(float lo, float hi) { return f2bf(lo) | (f2bf(hi) << 16); }
; #define CBAR() do { asm volatile("s_waitcnt lgkmcnt(0)" ::: "memory"); __builtin_amdgcn_s_barrier(); asm volatile("" ::: "memory"); } while (0)
; __device__ __forceinline__ void p4a_chunk(Frame& F0, const In& I) {
;     ...
;             *(LAS unsigned short*)(L + C_BT + t * CP + lane * 2) = (unsigned short)f2bf(Bv);
;             *(LAS unsigned short*)(L + C_KT + t * CP + lane * 2) = (unsigned short)f2bf(Kv); }
; #pragma unroll
;         for (int q = 0; q < 4; ++q) { att[q] = pk2(at_[2 * q], at_[2 * q + 1]); bht[q] = pk2(bh_[2 * q], bh_[2 * q + 1]); kht[q] = pk2(kh_[2 * q], kh_[2 * q + 1]); vtt[q] = pk2(vv[2 * q], vv[2 * q + 1]); }
;         *(LAS v4u*)(L + C_ATT + lane * CP + 16 * w) = (v4u){att[0], att[1], att[2], att[3]};
;         *(LAS v4u*)(L + C_WA + (64 + lane) * CP + 16 * w) = (v4u){bht[0], bht[1], bht[2], bht[3]};
;         CBAR();
;         const int cit = unit * 12 + w; const bool hx = cit < MOE_NITEMS, hy = (w < 4) && (cit + 8 < MOE_NITEMS);
;         f32x4 tX[16]; MoeItem mX = moe_item(hx ? cit : 0, I.w_gu, I.w_down, F.ws);
	v_mov_b32_e32 v178, s16
	v_mov_b32_e32 v179, s17
	v_pk_add_f32 v[178:179], s[14:15], v[178:179]
	v_max_f32_e32 v114, 0x179abe15, v114
	v_add_f32_e32 v115, v178, v179
	v_max_f32_e32 v115, 0x179abe15, v115
	v_rsq_f32_e32 v114, v114
	v_rsq_f32_e32 v115, v115
	v_lshrrev_b32_e32 v178, 16, v95
	v_lshrrev_b32_e32 v179, 16, v180
	s_and_b64 s[14:15], s[74:75], exec
	v_pk_mul_f32 v[114:115], v[88:89], v[114:115]
	s_cselect_b32 s15, s85, 0
	v_pk_mul_f32 v[88:89], v[112:113], v[114:115] neg_lo:[0,1] neg_hi:[0,1]
	v_pk_mul_f32 v[96:97], v[114:115], v[96:97]
	v_and_b32_sdwa v95, v89, v159 dst_sel:DWORD dst_unused:UNUSED_PAD src0_sel:WORD_1 src1_sel:DWORD
	v_and_b32_sdwa v112, v88, v159 dst_sel:DWORD dst_unused:UNUSED_PAD src0_sel:WORD_1 src1_sel:DWORD
	v_add3_u32 v113, v89, v95, s3
	v_add3_u32 v112, v88, v112, s3
	v_pk_fma_f32 v[88:89], v[106:107], v[68:69], 1.0 op_sel_hi:[1,0,0]
	ds_write_b16_d16_hi v194, v112 offset:56016
	ds_write_b16_d16_hi v194, v180 offset:56160
	ds_write_b16_d16_hi v194, v113 offset:56304
	v_pk_mul_f32 v[88:89], v[88:89], v[90:91]
	s_cmp_gt_i32 s15, 0xffff
	v_mul_f32_e32 v95, v88, v100
	v_bfe_u32 v106, v95, 16, 1
	v_pk_mul_f32 v[90:91], v[94:95], v[100:101] op_sel_hi:[0,1]
	v_add3_u32 v95, v95, v106, s3
	v_pk_fma_f32 v[106:107], v[110:111], v[68:69], 1.0 op_sel_hi:[1,0,0]
	ds_write_b16_d16_hi v71, v95 offset:576
	v_pk_mul_f32 v[92:93], v[106:107], v[92:93]
	v_pk_mul_f32 v[94:95], v[94:95], v[102:103] op_sel_hi:[0,1]
	v_mul_f32_e32 v68, v92, v102
	v_bfe_u32 v106, v68, 16, 1
	v_add3_u32 v68, v68, v106, s3
	ds_write_b16_d16_hi v71, v68 offset:720
	v_mul_f32_e32 v68, v89, v101
	v_bfe_u32 v106, v68, 16, 1
	v_add3_u32 v68, v68, v106, s3
	ds_write_b16_d16_hi v71, v68 offset:864
	v_mul_f32_e32 v68, v93, v103
	v_bfe_u32 v106, v68, 16, 1
	v_add3_u32 v68, v68, v106, s3
	ds_write_b16_d16_hi v71, v68 offset:1008
	v_mul_f32_e32 v68, v100, v98
	v_bfe_u32 v100, v68, 16, 1
	v_add3_u32 v68, v68, v100, s3
	ds_write_b16_d16_hi v194, v68 offset:65088
	v_mul_f32_e32 v68, v102, v96
	v_bfe_u32 v100, v68, 16, 1
	v_add3_u32 v68, v68, v100, s3
	ds_write_b16_d16_hi v194, v68 offset:65232
	v_mul_f32_e32 v68, v101, v99
	v_bfe_u32 v100, v68, 16, 1
	v_add3_u32 v68, v68, v100, s3
	ds_write_b16_d16_hi v194, v68 offset:65376
	v_mul_f32_e32 v68, v103, v97
	v_bfe_u32 v100, v68, 16, 1
	v_add3_u32 v68, v68, v100, s3
	v_pk_mul_f32 v[100:101], v[90:91], v[98:99]
	v_pk_mul_f32 v[102:103], v[94:95], v[96:97]
	v_and_or_b32 v99, v113, s4, v179
	v_and_or_b32 v98, v112, s4, v178
	v_and_or_b32 v97, v185, s4, v187
	v_and_or_b32 v96, v184, s4, v186
	ds_write_b16_d16_hi v194, v68 offset:65520
	ds_write_b128 v73, v[96:99] offset:9216
	v_bfe_u32 v68, v103, 16, 1
	v_bfe_u32 v96, v102, 16, 1
	v_bfe_u32 v98, v104, 16, 1
	v_add3_u32 v104, v104, v98, s3
	v_add3_u32 v96, v102, v96, s3
	v_add3_u32 v68, v103, v68, s3
	v_bfe_u32 v98, v108, 16, 1
	v_bfe_u32 v99, v109, 16, 1
	v_bfe_u32 v102, v100, 16, 1
	v_bfe_u32 v103, v101, 16, 1
	v_bfe_u32 v97, v105, 16, 1
	v_add3_u32 v101, v101, v103, s3
	v_add3_u32 v100, v100, v102, s3
	v_add3_u32 v99, v109, v99, s3
	v_add3_u32 v98, v108, v98, s3
	v_add3_u32 v97, v105, v97, s3
	v_lshrrev_b32_e32 v102, 16, v98
	v_lshrrev_b32_e32 v103, 16, v99
	v_lshrrev_b32_e32 v98, 16, v100
	v_lshrrev_b32_e32 v99, 16, v101
	v_and_or_b32 v99, v68, s4, v99
	v_and_or_b32 v98, v96, s4, v98
	v_and_or_b32 v97, v97, s4, v103
	v_and_or_b32 v96, v104, s4, v102
	ds_write_b128 v73, v[96:99] offset:46080
	s_waitcnt lgkmcnt(0)
	s_barrier
	s_cbranch_scc0 .LBB0_1087
	s_add_i32 s14, s15, 0xffff0000
	s_lshr_b32 s86, s14, 10
	s_bfe_u32 s14, s15, 0x50005
	s_lshl_b64 s[64:65], s[86:87], 22
	s_lshl_b32 s16, s14, 17
	s_lshl_b32 s17, s15, 6
	s_and_b32 s86, s17, 0x7c0
	s_or_b32 s16, s16, s64
	s_or_b32 s16, s16, s86
	s_add_u32 s72, s68, s64
	s_addc_u32 s73, s69, s65
	s_mov_b64 s[64:65], 0

; #define LAS __attribute__((address_space(3)))
; __device__ __forceinline__ unsigned f2bf(float f) { unsigned u = __builtin_bit_cast(unsigned, f); return (u + 0x7fffu + ((u >> 16) & 1u)) >> 16; }
; #define CBAR() do { asm volatile("s_waitcnt lgkmcnt(0)" ::: "memory"); __builtin_amdgcn_s_barrier(); asm volatile("" ::: "memory"); } while (0)
; __device__ __forceinline__ v2u pack4(const f32x4& v) { return (v2u){pg8::cvt_pk_bf16(v[0], v[1]), pg8::cvt_pk_bf16(v[2], v[3])}; }
; __device__ __forceinline__ void p4a_chunk(Frame& F0, const In& I) {
;     ...
;         { const Fr yAT = LD(C_AT, nt), yKT = LD(C_KT, nt), yRT = LD(C_RT, nt);
;           Fr xBT[2], xAT[2], xKT[2];
; #pragma unroll
;           for (int i = 0; i < 2; ++i) { xBT[i] = LD(C_BT, mt0 + i); xAT[i] = LD(C_AT, mt0 + i); xKT[i] = LD(C_KT, mt0 + i); }
;           f32x4 a1[2], a2[2], a3[2], a4[2];
; #pragma unroll
;           for (int i = 0; i < 2; ++i) { a1[i] = MM(xBT[i], yAT); a2[i] = MM(xAT[i], yKT); a3[i] = MM(xBT[i], yRT); a4[i] = MM(xKT[i], yRT); }
; #pragma unroll
;           for (int i = 0; i < 2; ++i) { const int m0 = (mt0 + i) * 16 + 4 * kq;
;               f32x4 v = a1[i];
; #pragma unroll
;               for (int e = 0; e < 4; ++e) { v[e] = (m0 + e < n) ? v[e] : 0.f; *(LAS unsigned short*)(L + C_MA + (m0 + e) * CP + n * 2) = (unsigned short)f2bf(v[e]); }
;               *(LAS v2u*)(L + C_MTA + n * CP + m0 * 2) = pack4(v);
;               v = a2[i];
; #pragma unroll
;               for (int e = 0; e < 4; ++e) v[e] = (n < m0 + e) ? v[e] : 0.f;
;               *(LAS v2u*)(L + C_AAK + n * CP + m0 * 2) = pack4(v);
;               v = a3[i];
; #pragma unroll
;               for (int e = 0; e < 4; ++e) v[e] = (m0 + e <= n) ? v[e] : 0.f;
;               *(LAS v2u*)(L + C_WA + n * CP + m0 * 2) = pack4(v);
;               v = a4[i];
; #pragma unroll
;               for (int e = 0; e < 4; ++e) v[e] = (m0 + e <= n) ? v[e] : 0.f;
;               *(LAS v2u*)(L + C_ARKT + n * CP + m0 * 2) = pack4(v); } }
;         CBAR();
;         if (hx) tr8_load(mX, tX, lane);
.LBB0_1090:
	v_add_u32_e32 v96, v124, v131
	ds_read_b128 v[98:101], v96 offset:64512
	ds_read_b128 v[102:105], v123 offset:55296
	ds_read_b128 v[106:109], v96 offset:55296
	ds_read_b128 v[110:113], v123 offset:55360
	ds_read_b128 v[176:179], v96 offset:64576
	ds_read_b128 v[184:187], v152
	ds_read_b128 v[188:191], v152 offset:64
	ds_read_b128 v[192:195], v96 offset:55360
	s_waitcnt lgkmcnt(6)
	v_mfma_f32_16x16x32_bf16 v[180:183], v[98:101], v[102:105], 0
	ds_read_b128 v[196:199], v123
	ds_read_b128 v[200:203], v123 offset:64
	v_add_u32_e32 v68, v125, v131
	v_add_u32_e32 v97, v124, v139
	s_waitcnt lgkmcnt(4)
	v_mfma_f32_16x16x32_bf16 v[106:109], v[106:109], v[184:187], 0
	s_mov_b64 s[92:93], s[20:21]
	v_readlane_b32 s20, v255, 30
	v_add_u32_e32 v115, v126, v140
	v_mfma_f32_16x16x32_bf16 v[180:183], v[176:179], v[110:113], v[180:183]
	v_readlane_b32 s21, v255, 31
	s_andn2_b64 vcc, exec, s[74:75]
	s_waitcnt lgkmcnt(1)
	v_mfma_f32_16x16x32_bf16 v[98:101], v[98:101], v[196:199], 0
	v_mfma_f32_16x16x32_bf16 v[106:109], v[192:195], v[188:191], v[106:109]
	ds_read_b128 v[192:195], v68
	ds_read_b128 v[204:207], v68 offset:64
	ds_read_b128 v[208:211], v97 offset:64512
	ds_read_b128 v[212:215], v97 offset:64576
	v_add_u32_e32 v68, v125, v139
	s_waitcnt lgkmcnt(4)
	v_mfma_f32_16x16x32_bf16 v[176:179], v[176:179], v[200:203], v[98:101]
	s_nop 2
	ds_read_b128 v[98:101], v97 offset:55296
	ds_read_b128 v[216:219], v97 offset:55360
	ds_read_b128 v[220:223], v68
	ds_read_b128 v[224:227], v68 offset:64
	v_cndmask_b32_e64 v68, 0, v180, s[18:19]
	v_bfe_u32 v114, v68, 16, 1
	s_waitcnt lgkmcnt(5)
	v_mfma_f32_16x16x32_bf16 v[102:105], v[208:211], v[102:105], 0
	v_add3_u32 v114, v68, v114, s3
	ds_write_b16_d16_hi v115, v114
	v_cndmask_b32_e64 v114, 0, v181, s[20:21]
	v_bfe_u32 v180, v114, 16, 1
	v_readlane_b32 s20, v255, 32
	s_waitcnt lgkmcnt(5)
	v_mfma_f32_16x16x32_bf16 v[102:105], v[212:215], v[110:113], v[102:105]
	v_add3_u32 v110, v114, v180, s3
	v_readlane_b32 s21, v255, 33
	ds_write_b16_d16_hi v115, v110 offset:144
	s_waitcnt lgkmcnt(5)
	v_mfma_f32_16x16x32_bf16 v[98:101], v[98:101], v[184:187], 0
	v_cndmask_b32_e64 v115, 0, v182, s[20:21]
	v_readlane_b32 s20, v255, 34
	v_bfe_u32 v110, v115, 16, 1
	v_readlane_b32 s21, v255, 35
	v_add3_u32 v110, v115, v110, s3
	ds_write_b16_d16_hi v153, v110
	v_cndmask_b32_e64 v180, 0, v183, s[20:21]
	s_waitcnt lgkmcnt(5)
	v_mfma_f32_16x16x32_bf16 v[110:113], v[216:219], v[188:191], v[98:101]
	v_cvt_pk_bf16_f32 v114, v68, v114
	v_cvt_pk_bf16_f32 v115, v115, v180
	v_cndmask_b32_e64 v68, 0, v106, s[26:27]
	v_bfe_u32 v98, v180, 16, 1
	v_mfma_f32_16x16x32_bf16 v[192:195], v[192:195], v[196:199], 0
	v_add3_u32 v181, v180, v98, s3
	ds_write_b16_d16_hi v154, v181
	v_readlane_b32 s20, v255, 36
	v_mfma_f32_16x16x32_bf16 v[98:101], v[208:211], v[196:199], 0
	v_readlane_b32 s21, v255, 37
	v_mfma_f32_16x16x32_bf16 v[192:195], v[204:207], v[200:203], v[192:195]
	v_mfma_f32_16x16x32_bf16 v[180:183], v[212:215], v[200:203], v[98:101]
	s_nop 4
	v_add_u32_e32 v99, v127, v141
	ds_write_b64 v99, v[114:115]
	v_cndmask_b32_e64 v98, v107, 0, s[18:19]
	v_cndmask_b32_e64 v101, 0, v108, s[28:29]
	v_cndmask_b32_e64 v114, 0, v109, s[30:31]
	v_cvt_pk_bf16_f32 v100, v68, v98
	v_cvt_pk_bf16_f32 v101, v101, v114
	v_cndmask_b32_e64 v98, v176, 0, s[26:27]
	v_cndmask_b32_e64 v114, 0, v177, s[18:19]
	v_cndmask_b32_e64 v115, v178, 0, s[28:29]
	v_cndmask_b32_e64 v176, v179, 0, s[30:31]
	v_add_u32_e32 v68, v121, v141
	v_cvt_pk_bf16_f32 v114, v98, v114
	v_cvt_pk_bf16_f32 v115, v115, v176
	ds_write_b64 v68, v[114:115] offset:36864
	v_cndmask_b32_e64 v98, v192, 0, s[26:27]
	v_cndmask_b32_e64 v114, 0, v193, s[18:19]
	v_cndmask_b32_e64 v115, v194, 0, s[28:29]
	v_cndmask_b32_e64 v176, v195, 0, s[30:31]
	v_cvt_pk_bf16_f32 v114, v98, v114
	v_cvt_pk_bf16_f32 v115, v115, v176
	ds_write2st64_b64 v68, v[100:101], v[114:115] offset0:36 offset1:54
	v_cndmask_b32_e64 v68, 0, v102, s[34:35]
	v_bfe_u32 v98, v68, 16, 1
	v_add3_u32 v98, v68, v98, s3
	v_add_u32_e32 v100, v126, v142
	ds_write_b16_d16_hi v100, v98
	v_cndmask_b32_e64 v98, 0, v103, s[20:21]
	v_bfe_u32 v101, v98, 16, 1
	v_readlane_b32 s20, v255, 38
	v_add3_u32 v101, v98, v101, s3
	v_readlane_b32 s21, v255, 39
	ds_write_b16_d16_hi v100, v101 offset:144
	s_waitcnt lgkmcnt(10)
	v_mfma_f32_16x16x32_bf16 v[184:187], v[220:223], v[196:199], 0
	v_cndmask_b32_e64 v101, 0, v104, s[20:21]
	v_readlane_b32 s20, v255, 40
	v_bfe_u32 v100, v101, 16, 1
	v_readlane_b32 s21, v255, 41
	v_add3_u32 v100, v101, v100, s3
	ds_write_b16_d16_hi v155, v100
	v_cndmask_b32_e64 v102, 0, v105, s[20:21]
	v_bfe_u32 v100, v102, 16, 1
	v_add3_u32 v100, v102, v100, s3
	s_waitcnt lgkmcnt(10)
	v_mfma_f32_16x16x32_bf16 v[106:109], v[224:227], v[200:203], v[184:187]
	ds_write_b16_d16_hi v156, v100
	v_cvt_pk_bf16_f32 v100, v68, v98
	v_cvt_pk_bf16_f32 v101, v101, v102
	v_add_u32_e32 v98, v127, v143
	ds_write_b64 v98, v[100:101]
	v_cndmask_b32_e64 v101, 0, v112, s[44:45]
	v_cndmask_b32_e64 v102, 0, v113, s[46:47]
	v_cndmask_b32_e64 v68, 0, v110, s[42:43]
	v_cndmask_b32_e64 v100, v111, 0, s[34:35]
	v_cvt_pk_bf16_f32 v101, v101, v102
	v_cndmask_b32_e64 v102, v180, 0, s[42:43]
	v_cndmask_b32_e64 v103, 0, v181, s[34:35]
	v_cndmask_b32_e64 v104, v182, 0, s[44:45]
	v_cndmask_b32_e64 v105, v183, 0, s[46:47]
	v_cvt_pk_bf16_f32 v100, v68, v100
	v_add_u32_e32 v68, v121, v143
	v_cvt_pk_bf16_f32 v102, v102, v103
	v_cvt_pk_bf16_f32 v103, v104, v105
	ds_write_b64 v68, v[102:103] offset:36864
	v_cndmask_b32_e64 v102, v106, 0, s[42:43]
	v_cndmask_b32_e64 v103, 0, v107, s[34:35]
	v_cndmask_b32_e64 v104, v108, 0, s[44:45]
	v_cndmask_b32_e64 v105, v109, 0, s[46:47]
	v_cvt_pk_bf16_f32 v102, v102, v103
	v_cvt_pk_bf16_f32 v103, v104, v105
	ds_write2st64_b64 v68, v[100:101], v[102:103] offset0:36 offset1:54
	s_waitcnt lgkmcnt(0)
	s_barrier
	v_cndmask_b32_e64 v68, 0, 1, s[74:75]
	v_cmp_ne_u32_e64 s[64:65], 1, v68
	s_cbranch_vccnz .LBB0_1092
	s_lshl_b32 s74, s16, 2
	s_add_i32 s16, s15, s16
	s_add_i32 s17, s15, s74
	s_lshl_b32 s16, s16, 2
	s_add_i32 s17, s17, s15
	s_add_i32 s17, s17, s15
	s_lshl_b32 s16, s15, 1
	s_add_i32 s16, s17, s16
	s_add_i32 s16, s16, s15
	s_add_i32 s16, s16, s15
	s_add_i32 s16, s16, s15
	s_add_i32 s16, s16, s15
	s_add_i32 s16, s16, s15
	s_add_i32 s16, s16, s15
	s_add_i32 s16, s16, s15
	s_add_i32 s16, s16, s15
	s_add_i32 s16, s16, s15
	s_add_i32 s16, s16, s15

; #define GAS __attribute__((address_space(1)))
; __device__ __forceinline__ void p5_post(Frame& F0, const In& I) {
;     ...
;     float p_ka[16], p_rk[16], p_lw[16], p_lb[16];
; #pragma unroll
;     for (int q = 0; q < 4; ++q) { const f32x4 a = *(const GAS f32x4*)(I.k_a + c0 + 4 * q), bq = *(const GAS f32x4*)(I.r_k + c0 + 4 * q), c = *(const GAS f32x4*)(I.lnx_w + c0 + 4 * q), d = *(const GAS f32x4*)(I.lnx_b + c0 + 4 * q);
; #pragma unroll
;         for (int e = 0; e < 4; ++e) { p_ka[4 * q + e] = a[e]; p_rk[4 * q + e] = bq[e]; p_lw[4 * q + e] = c[e]; p_lb[4 * q + e] = d[e]; } }
;     v4u raw[12];
;     ...
;     if (gw < T) P5_LOAD(gw);
.LBB0_1211:
	s_or_b64 exec, exec, s[0:1]
	s_waitcnt lgkmcnt(0)
	v_mov_b32_e32 v1, v0
	s_barrier
	v_readlane_b32 s1, v254, 53
	v_readfirstlane_b32 s0, v1
	s_ashr_i32 s0, s0, 6
	s_add_i32 s2, s0, s1
	s_cmpk_gt_i32 s2, 0x7fff
	s_cbranch_scc1 .LBB0_1216
	s_ashr_i32 s3, s2, 31
	s_lshl_b64 s[6:7], s[2:3], 11
	s_add_u32 s4, s96, s6
	s_addc_u32 s5, s97, s7
	v_lshlrev_b32_e32 v2, 4, v1
	s_add_u32 s8, s88, s6
	v_and_b32_e32 v68, 0x3f0, v2
	v_mov_b32_e32 v162, 0
	s_addc_u32 s9, s89, s7
	s_mul_i32 s3, s2, 0x1800
	v_readlane_b32 s10, v254, 54
	v_lshlrev_b32_e32 v58, 1, v68
	v_mov_b32_e32 v59, v162
	s_mul_hi_i32 s1, s2, 0x1800
	v_readlane_b32 s11, v254, 55
	s_add_u32 s10, s10, s3
	v_lshl_add_u64 v[60:61], s[4:5], 0, v[58:59]
	s_mov_b64 s[4:5], 0x90000000
	s_addc_u32 s11, s11, s1
	s_brev_b32 s1, 9
	v_readlane_b32 s12, v254, 21
	v_lshl_add_u64 v[62:63], v[60:61], 0, s[4:5]
	v_add_co_u32_e32 v60, vcc, s1, v60
	v_lshlrev_b32_e32 v69, 2, v68
	v_readlane_b32 s16, v254, 25
	v_readlane_b32 s17, v254, 26
	v_lshl_add_u64 v[64:65], s[10:11], 0, v[58:59]
	v_addc_co_u32_e32 v61, vcc, 0, v61, vcc
	s_movk_i32 s1, 0x1000
	v_readlane_b32 s13, v254, 22
	v_readlane_b32 s18, v254, 27
	v_readlane_b32 s19, v254, 28
	v_readlane_b32 s20, v254, 29
	v_readlane_b32 s21, v254, 30
	v_readlane_b32 s22, v254, 31
	v_readlane_b32 s23, v254, 32
	global_load_dwordx4 v[2:5], v69, s[16:17]
	global_load_dwordx4 v[6:9], v69, s[18:19]
	global_load_dwordx4 v[10:13], v69, s[16:17] offset:16
	global_load_dwordx4 v[14:17], v69, s[18:19] offset:16
	global_load_dwordx4 v[18:21], v69, s[16:17] offset:32
	global_load_dwordx4 v[22:25], v69, s[18:19] offset:32
	global_load_dwordx4 v[26:29], v69, s[20:21]
	global_load_dwordx4 v[30:33], v69, s[22:23]
	global_load_dwordx4 v[34:37], v69, s[20:21] offset:16
	global_load_dwordx4 v[38:41], v69, s[22:23] offset:16
	global_load_dwordx4 v[42:45], v69, s[20:21] offset:32
	global_load_dwordx4 v[46:49], v69, s[22:23] offset:32
	global_load_dwordx4 v[50:53], v69, s[20:21] offset:48
	global_load_dwordx4 v[54:57], v69, s[22:23] offset:48
	global_load_dwordx4 v[134:137], v[60:61], off
	global_load_dwordx4 v[114:117], v[62:63], off offset:16
	global_load_dwordx4 v[118:121], v58, s[8:9] offset:16
	global_load_dwordx4 v[142:145], v58, s[8:9]
	global_load_dwordx4 v[122:125], v58, s[10:11] offset:16
	global_load_dwordx4 v[146:149], v58, s[10:11]
	global_load_dwordx4 v[126:129], v58, s[10:11] offset:2064
	global_load_dwordx4 v[150:153], v58, s[10:11] offset:2048
	v_add_co_u32_e32 v60, vcc, s1, v64
	s_mov_b64 s[12:13], 0x1000
	s_add_u32 s6, s66, s6
	v_addc_co_u32_e32 v61, vcc, 0, v65, vcc
	v_lshl_add_u64 v[66:67], v[64:65], 0, s[12:13]
	s_addc_u32 s7, s67, s7
	global_load_dwordx4 v[154:157], v[60:61], off
	global_load_dwordx4 v[130:133], v[66:67], off offset:16
	global_load_dwordx4 v[138:141], v58, s[6:7] offset:16
	global_load_dwordx4 v[158:161], v58, s[6:7]
	s_nop 0
	global_load_dwordx4 v[58:61], v69, s[18:19] offset:48
	global_load_dwordx4 v[62:65], v69, s[16:17] offset:48
	v_readlane_b32 s6, v254, 53
	s_ashr_i32 s1, s0, 31
	s_ashr_i32 s3, s6, 31
	s_add_u32 s0, s0, s6
	s_addc_u32 s1, s1, s3
	s_add_i32 s12, s2, s68
	s_lshl_b64 s[0:1], s[0:1], 10
	s_mov_b64 s[8:9], 0x98000000
	v_lshlrev_b32_e32 v1, 5, v1
	s_ashr_i32 s13, s12, 31
	v_or_b32_e32 v66, s0, v68
	v_mov_b32_e32 v67, s1
	v_readlane_b32 s14, v254, 23
	v_readlane_b32 s15, v254, 24
	v_and_b32_e32 v1, 0x7e0, v1
	s_ashr_i32 s69, s68, 31
	s_mul_hi_i32 s3, s12, 0x1800
	s_mul_i32 s10, s12, 0x1800
	v_lshl_add_u64 v[166:167], v[66:67], 0, s[8:9]
	s_lshl_b64 s[0:1], s[12:13], 11
	s_lshl_b64 s[6:7], s[68:69], 10
	v_or_b32_e32 v164, s10, v1
	v_mov_b32_e32 v165, s3
	s_mul_hi_i32 s11, s68, 0x1800
	s_mul_i32 s10, s68, 0x1800
	v_or_b32_e32 v170, s0, v1
	v_mov_b32_e32 v171, s1
	s_lshl_b64 s[12:13], s[68:69], 11
	s_mov_b64 s[14:15], 0x84000000
	s_mov_b64 s[16:17], 0x6e000000
	s_mov_b64 s[18:19], 0x6e000800
	s_mov_b64 s[20:21], 0x6e001000
	s_mov_b64 s[22:23], 0x8c000000
	s_mov_b32 s3, 0x6e001000
	v_mov_b32_e32 v1, 0x3a27c5ac
	s_mov_b32 s8, 0xf800000
	v_mov_b32_e32 v173, 0x3c800000
	v_readlane_b32 s24, v254, 33
	v_readlane_b32 s25, v254, 34
	v_readlane_b32 s26, v254, 35
	v_readlane_b32 s27, v254, 36
	s_waitcnt vmcnt(13)
	v_mov_b64_e32 v[66:67], v[134:135]
	s_waitcnt vmcnt(12)
	v_mov_b64_e32 v[70:71], v[114:115]
	s_waitcnt vmcnt(11)
	v_mov_b64_e32 v[78:79], v[118:119]
	s_waitcnt vmcnt(10)
	v_mov_b64_e32 v[74:75], v[142:143]
	s_waitcnt vmcnt(9)
	v_mov_b64_e32 v[86:87], v[122:123]
	s_waitcnt vmcnt(8)
	v_mov_b64_e32 v[82:83], v[146:147]
	s_waitcnt vmcnt(7)
	v_mov_b64_e32 v[94:95], v[126:127]
	s_waitcnt vmcnt(6)
	v_mov_b64_e32 v[90:91], v[150:151]
	v_mov_b32_e32 v169, v52
	v_mov_b32_e32 v52, 0x260
	v_mov_b64_e32 v[68:69], v[136:137]
	s_waitcnt vmcnt(5)
	v_mov_b64_e32 v[98:99], v[154:155]
	s_waitcnt vmcnt(4)
	v_mov_b64_e32 v[102:103], v[130:131]
	s_waitcnt vmcnt(3)
	v_mov_b64_e32 v[110:111], v[138:139]
	s_waitcnt vmcnt(2)
	v_mov_b64_e32 v[106:107], v[158:159]
	v_mov_b64_e32 v[72:73], v[116:117]
	v_mov_b64_e32 v[76:77], v[144:145]
	v_mov_b64_e32 v[80:81], v[120:121]
	v_mov_b64_e32 v[84:85], v[148:149]
	v_mov_b64_e32 v[88:89], v[124:125]
	v_mov_b64_e32 v[92:93], v[152:153]
	v_mov_b64_e32 v[96:97], v[128:129]
	v_mov_b64_e32 v[100:101], v[156:157]
	v_mov_b64_e32 v[104:105], v[132:133]
	v_mov_b64_e32 v[108:109], v[160:161]
	v_mov_b64_e32 v[112:113], v[140:141]
	s_waitcnt vmcnt(0)
	s_branch .LBB0_1214
; __device__ __forceinline__ void p5_post(Frame& F0, const In& I) {
;     ...
;     for (int tok = gw; tok < T; tok += NGW) {
;         float y[16], rr[16], kk[16], vv[16], ic[16], gg[16];
; #pragma unroll
;         for (int q = 0; q < 2; ++q) {
;             const unsigned yw[4] = {raw[q].x, raw[q].y, raw[q].z, raw[q].w}, iw[4] = {raw[2 + q].x, raw[2 + q].y, raw[2 + q].z, raw[2 + q].w};
;             const unsigned aw[4] = {raw[4 + q].x, raw[4 + q].y, raw[4 + q].z, raw[4 + q].w}, bw[4] = {raw[6 + q].x, raw[6 + q].y, raw[6 + q].z, raw[6 + q].w};
;             const unsigned cw[4] = {raw[8 + q].x, raw[8 + q].y, raw[8 + q].z, raw[8 + q].w}, dw[4] = {raw[10 + q].x, raw[10 + q].y, raw[10 + q].z, raw[10 + q].w};
; #pragma unroll
;             for (int e = 0; e < 4; ++e) { y[8 * q + 2 * e] = bflo(yw[e]); y[8 * q + 2 * e + 1] = bfhi(yw[e]); ic[8 * q + 2 * e] = bflo(iw[e]); ic[8 * q + 2 * e + 1] = bfhi(iw[e]);
;                 rr[8 * q + 2 * e] = bflo(aw[e]); rr[8 * q + 2 * e + 1] = bfhi(aw[e]); kk[8 * q + 2 * e] = bflo(bw[e]); kk[8 * q + 2 * e + 1] = bfhi(bw[e]);
;                 vv[8 * q + 2 * e] = bflo(cw[e]); vv[8 * q + 2 * e + 1] = bfhi(cw[e]); gg[8 * q + 2 * e] = bflo(dw[e]); gg[8 * q + 2 * e + 1] = bfhi(dw[e]); } }
;         __builtin_amdgcn_sched_barrier(0);
;         if (tok + NGW < T) P5_LOAD(tok + NGW);
;         __builtin_amdgcn_sched_barrier(0);
;         float s = 0.f, bs = 0.f;
; #pragma unroll
;         for (int e = 0; e < 16; ++e) { s += y[e]; const float kp = kk[e] * (1.0f + (ic[e] - 1.0f) * p_ka[e]); bs += rr[e] * kp * p_rk[e]; }
.LBB0_1213:
	v_lshlrev_b32_e32 v198, 16, v134
	v_lshlrev_b32_e32 v172, 16, v142
	v_and_b32_e32 v176, 0xffff0000, v142
	v_lshlrev_b32_e32 v190, 16, v146
	v_and_b32_e32 v175, 0xffff0000, v134
	v_and_b32_e32 v178, 0xffff0000, v146
	v_lshlrev_b32_e32 v180, 16, v150
	v_and_b32_e32 v182, 0xffff0000, v150
	v_lshlrev_b32_e32 v174, 16, v154
	v_and_b32_e32 v150, 0xffff0000, v154
	v_lshlrev_b32_e32 v177, 16, v135
	v_and_b32_e32 v163, 0xffff0000, v135
	v_lshlrev_b32_e32 v135, 16, v143
	v_and_b32_e32 v143, 0xffff0000, v143
	v_lshlrev_b32_e32 v192, 16, v147
	v_and_b32_e32 v147, 0xffff0000, v147
	v_lshlrev_b32_e32 v201, 16, v151
	v_and_b32_e32 v151, 0xffff0000, v151
	v_lshlrev_b32_e32 v154, 16, v155
	v_and_b32_e32 v146, 0xffff0000, v155
	v_lshlrev_b32_e32 v202, 16, v159
	v_and_b32_e32 v203, 0xffff0000, v159
	v_lshlrev_b32_e32 v159, 16, v136
	v_and_b32_e32 v179, 0xffff0000, v136
	v_lshlrev_b32_e32 v155, 16, v144
	v_and_b32_e32 v204, 0xffff0000, v144
	v_lshlrev_b32_e32 v205, 16, v148
	v_and_b32_e32 v206, 0xffff0000, v148
	v_lshlrev_b32_e32 v207, 16, v152
	v_and_b32_e32 v152, 0xffff0000, v152
	v_lshlrev_b32_e32 v148, 16, v156
	v_and_b32_e32 v142, 0xffff0000, v156
	v_lshlrev_b32_e32 v208, 16, v160
	v_and_b32_e32 v209, 0xffff0000, v160
	v_lshlrev_b32_e32 v181, 16, v137
	v_and_b32_e32 v183, 0xffff0000, v137
	v_lshlrev_b32_e32 v137, 16, v145
	v_and_b32_e32 v145, 0xffff0000, v145
	v_lshlrev_b32_e32 v156, 16, v149
	v_and_b32_e32 v149, 0xffff0000, v149
	v_lshlrev_b32_e32 v160, 16, v153
	v_and_b32_e32 v210, 0xffff0000, v153
	v_lshlrev_b32_e32 v144, 16, v157
	v_and_b32_e32 v134, 0xffff0000, v157
	v_lshlrev_b32_e32 v211, 16, v161
	v_and_b32_e32 v212, 0xffff0000, v161
	v_lshlrev_b32_e32 v153, 16, v114
	v_and_b32_e32 v157, 0xffff0000, v114
	v_lshlrev_b32_e32 v213, 16, v118
	v_and_b32_e32 v214, 0xffff0000, v118
	v_lshlrev_b32_e32 v215, 16, v122
	v_and_b32_e32 v216, 0xffff0000, v122
	v_lshlrev_b32_e32 v217, 16, v126
	v_and_b32_e32 v218, 0xffff0000, v126
	v_lshlrev_b32_e32 v136, 16, v130
	v_and_b32_e32 v126, 0xffff0000, v130
	v_lshlrev_b32_e32 v219, 16, v138
	v_and_b32_e32 v220, 0xffff0000, v138
	v_lshlrev_b32_e32 v161, 16, v115
	v_lshlrev_b32_e32 v138, 16, v119
	v_and_b32_e32 v119, 0xffff0000, v119
	v_lshlrev_b32_e32 v221, 16, v123
	v_and_b32_e32 v123, 0xffff0000, v123
	v_lshlrev_b32_e32 v222, 16, v127
	v_and_b32_e32 v127, 0xffff0000, v127
	v_lshlrev_b32_e32 v122, 16, v131
	v_and_b32_e32 v114, 0xffff0000, v131
	v_lshlrev_b32_e32 v223, 16, v139
	v_and_b32_e32 v224, 0xffff0000, v139
	v_lshlrev_b32_e32 v131, 16, v116
	v_and_b32_e32 v130, 0xffff0000, v115
	v_and_b32_e32 v139, 0xffff0000, v116
	v_and_b32_e32 v185, 0xffff0000, v120
	v_lshlrev_b32_e32 v184, 16, v120
	v_and_b32_e32 v187, 0xffff0000, v124
	v_lshlrev_b32_e32 v186, 16, v124
	v_lshlrev_b32_e32 v120, 16, v132
	v_and_b32_e32 v116, 0xffff0000, v132
	v_and_b32_e32 v197, 0xffff0000, v125
	v_lshlrev_b32_e32 v196, 16, v125
	v_and_b32_e32 v125, 0xffff0000, v129
	v_lshlrev_b32_e32 v124, 16, v129
	v_and_b32_e32 v118, 0xffff0000, v133
	v_lshlrev_b32_e32 v199, 16, v158
	v_and_b32_e32 v200, 0xffff0000, v158
	v_and_b32_e32 v189, 0xffff0000, v128
	v_lshlrev_b32_e32 v188, 16, v128
	v_lshlrev_b32_e32 v225, 16, v140
	v_and_b32_e32 v226, 0xffff0000, v140
	v_lshlrev_b32_e32 v191, 16, v117
	v_and_b32_e32 v193, 0xffff0000, v117
	v_and_b32_e32 v195, 0xffff0000, v121
	v_lshlrev_b32_e32 v194, 16, v121
	v_lshlrev_b32_e32 v168, 16, v133
	v_lshlrev_b32_e32 v227, 16, v141
	v_and_b32_e32 v228, 0xffff0000, v141
	v_add_f32_e32 v121, -1.0, v176
	v_fma_f32 v121, v3, v121, 1.0
	v_mul_f32_e32 v121, v121, v182
	v_mul_f32_e32 v121, v121, v178
	v_mul_f32_e32 v158, v7, v121
	v_add_f32_e32 v121, -1.0, v135
	v_fma_f32 v121, v4, v121, 1.0
	v_mul_f32_e32 v121, v121, v201
	v_mul_f32_e32 v121, v121, v192
	v_mul_f32_e32 v178, v8, v121
	v_add_f32_e32 v121, -1.0, v143
	v_fma_f32 v121, v5, v121, 1.0
	v_add_f32_e32 v117, -1.0, v172
	v_mul_f32_e32 v121, v121, v151
	v_fma_f32 v117, v2, v117, 1.0
	v_mul_f32_e32 v121, v121, v147
	v_mul_f32_e32 v117, v117, v180
	v_mul_f32_e32 v180, v9, v121
	v_add_f32_e32 v121, -1.0, v155
	v_fma_f32 v121, v10, v121, 1.0
	v_mul_f32_e32 v121, v121, v207
	v_mul_f32_e32 v121, v121, v205
	v_add_f32_e32 v115, 0, v198
	v_mul_f32_e32 v182, v14, v121
	v_add_f32_e32 v121, -1.0, v204
	v_fma_f32 v121, v11, v121, 1.0
	v_add_f32_e32 v115, v115, v175
	v_mov_b32_e32 v176, v6
	v_mul_f32_e32 v121, v121, v152
	v_pk_add_f32 v[132:133], v[176:177], v[114:115]
	v_add_f32_e32 v115, -1.0, v145
	v_mul_f32_e32 v121, v121, v206
	v_fma_f32 v115, v13, v115, 1.0
	v_mul_f32_e32 v152, v15, v121
	v_add_f32_e32 v121, -1.0, v137
	v_mul_f32_e32 v115, v115, v210
	v_fma_f32 v121, v12, v121, 1.0
	v_mul_f32_e32 v115, v115, v149
	v_mul_f32_e32 v121, v121, v160
	v_mul_f32_e32 v160, v17, v115
	v_add_f32_e32 v115, -1.0, v213
	v_fma_f32 v115, v18, v115, 1.0
	v_mul_f32_e32 v115, v115, v217
	v_mul_f32_e32 v128, v117, v190
	v_mul_f32_e32 v115, v115, v215
	v_pk_mul_f32 v[128:129], v[6:7], v[128:129]
	v_mul_f32_e32 v132, v22, v115
	v_add_f32_e32 v115, -1.0, v214
	v_mov_b32_e32 v129, v133
	v_fma_f32 v115, v19, v115, 1.0
	v_pk_add_f32 v[128:129], v[128:129], v[162:163]
	v_mul_f32_e32 v115, v115, v218
	v_pk_add_f32 v[128:129], v[128:129], v[158:159]
	v_mul_f32_e32 v115, v115, v216
	v_pk_add_f32 v[128:129], v[128:129], v[178:179]
	v_mul_f32_e32 v140, v23, v115
	v_add_f32_e32 v115, -1.0, v138
	v_pk_add_f32 v[128:129], v[128:129], v[180:181]
	v_fma_f32 v115, v20, v115, 1.0
	v_mul_f32_e32 v121, v121, v156
	v_pk_add_f32 v[128:129], v[128:129], v[182:183]
	v_mul_f32_e32 v115, v115, v222
	v_mul_f32_e32 v156, v16, v121
	v_mul_f32_e32 v115, v115, v221
	v_pk_add_f32 v[128:129], v[128:129], v[152:153]
; __device__ __forceinline__ float quadsum(float x) { x += dpp_f(x, 0); x += dpp_f(x, 1); return x; }
; __device__ __forceinline__ void p5_post(Frame& F0, const In& I) {
;     ...
;         for (int e = 0; e < 16; ++e) { s += y[e]; const float kp = kk[e] * (1.0f + (ic[e] - 1.0f) * p_ka[e]); bs += rr[e] * kp * p_rk[e]; }
;         s = quadsum(s); bs = quadsum(bs);
;         const float mean = s * (1.f / 64.f); float s2 = 0.f;
; #pragma unroll
;         for (int e = 0; e < 16; ++e) { y[e] -= mean; s2 += y[e] * y[e]; }
;         s2 = quadsum(s2);
;         const float rstd = 1.f / sqrtf(s2 * (1.f / 64.f) + GN_EPS);
	v_mul_f32_e32 v138, v24, v115
	v_add_f32_e32 v115, -1.0, v119
	v_pk_add_f32 v[184:185], v[184:185], -1.0 op_sel_hi:[1,0]
	v_pk_add_f32 v[128:129], v[128:129], v[156:157]
	v_fma_f32 v115, v21, v115, 1.0
	v_pk_fma_f32 v[184:185], v[62:63], v[184:185], 1.0 op_sel_hi:[1,1,0]
	v_pk_add_f32 v[128:129], v[128:129], v[160:161]
	v_mov_b32_e32 v133, v130
	v_mul_f32_e32 v115, v115, v127
	v_pk_mul_f32 v[184:185], v[184:185], v[188:189]
	v_pk_add_f32 v[128:129], v[128:129], v[132:133]
	v_mov_b32_e32 v141, v131
	v_mul_f32_e32 v115, v115, v123
	v_pk_mul_f32 v[184:185], v[184:185], v[186:187]
	v_pk_add_f32 v[128:129], v[128:129], v[140:141]
	v_mul_f32_e32 v190, v25, v115
	v_pk_mul_f32 v[184:185], v[58:59], v[184:185]
	v_pk_add_f32 v[186:187], v[194:195], -1.0 op_sel_hi:[1,0]
	v_pk_add_f32 v[128:129], v[128:129], v[138:139]
	v_pk_fma_f32 v[186:187], v[64:65], v[186:187], 1.0 op_sel_hi:[1,1,0]
	v_pk_add_f32 v[128:129], v[128:129], v[190:191]
	v_mov_b32_e32 v192, v184
	v_pk_mul_f32 v[124:125], v[186:187], v[124:125]
	v_pk_add_f32 v[128:129], v[192:193], v[128:129]
	v_mov_b32_e32 v133, v162
	v_pk_mul_f32 v[124:125], v[124:125], v[196:197]
	v_mov_b32_e32 v132, v185
	v_mov_b32_dpp v133, v129 quad_perm:[1,0,3,2] row_mask:0xf bank_mask:0xf
	v_pk_mul_f32 v[124:125], v[60:61], v[124:125]
	v_pk_add_f32 v[128:129], v[132:133], v[128:129]
	v_mov_b32_e32 v133, v162
	v_mov_b32_e32 v132, v124
	v_mov_b32_e32 v172, v125
	v_mov_b32_dpp v133, v129 quad_perm:[2,3,0,1] row_mask:0xf bank_mask:0xf
	v_pk_add_f32 v[128:129], v[132:133], v[128:129]
	v_mov_b32_e32 v190, v162
	v_pk_add_f32 v[124:125], v[172:173], v[128:129]
	v_pk_mul_f32 v[132:133], v[172:173], v[128:129]
	v_pk_fma_f32 v[128:129], v[172:173], v[128:129], v[174:175] neg_lo:[1,0,0] neg_hi:[1,0,0]
	v_sub_f32_e32 v115, v198, v133
	v_mul_f32_e32 v117, v129, v129
	v_fmac_f32_e32 v117, v115, v115
	v_sub_f32_e32 v119, v177, v133
	v_fmac_f32_e32 v117, v119, v119
	v_sub_f32_e32 v121, v163, v133
	v_fmac_f32_e32 v117, v121, v121
	v_sub_f32_e32 v123, v159, v133
	v_fmac_f32_e32 v117, v123, v123
	v_sub_f32_e32 v127, v179, v133
	v_fmac_f32_e32 v117, v127, v127
	v_sub_f32_e32 v135, v181, v133
	v_fmac_f32_e32 v117, v135, v135
	v_sub_f32_e32 v137, v183, v133
	v_fmac_f32_e32 v117, v137, v137
	v_sub_f32_e32 v152, v153, v133
	v_fmac_f32_e32 v117, v152, v152
	v_sub_f32_e32 v153, v157, v133
	v_mov_b32_e32 v125, v133
	v_mov_b32_dpp v190, v124 quad_perm:[1,0,3,2] row_mask:0xf bank_mask:0xf
	v_fmac_f32_e32 v117, v153, v153
	v_sub_f32_e32 v156, v161, v133
	v_pk_add_f32 v[130:131], v[130:131], v[132:133] op_sel:[0,1] neg_lo:[0,1] neg_hi:[0,1]
	v_fmac_f32_e32 v117, v156, v156
	v_pk_mul_f32 v[140:141], v[130:131], v[130:131]
	v_sub_f32_e32 v139, v139, v133
	v_sub_f32_e32 v157, v193, v133
	v_pk_add_f32 v[132:133], v[190:191], v[124:125] neg_lo:[0,1] neg_hi:[0,1]
	v_add_f32_e32 v117, v140, v117
	v_mov_b32_e32 v138, v133
	v_add_f32_e32 v117, v141, v117
	v_pk_mul_f32 v[140:141], v[138:139], v[138:139]
	v_pk_add_f32 v[124:125], v[124:125], v[190:191]
	v_add_f32_e32 v117, v141, v117
	v_add_f32_e32 v117, v140, v117
	v_fmac_f32_e32 v117, v157, v157
	v_lshl_add_u64 v[164:165], v[164:165], 0, s[10:11]
	v_add_f32_dpp v117, v117, v117 quad_perm:[1,0,3,2] row_mask:0xf bank_mask:0xf bound_ctrl:1
	v_lshl_add_u64 v[170:171], v[170:171], 0, s[12:13]
	v_add_f32_dpp v117, v117, v117 quad_perm:[2,3,0,1] row_mask:0xf bank_mask:0xf bound_ctrl:1
	v_fmamk_f32 v117, v117, 0x3c800000, v1
	v_mul_f32_e32 v128, 0x4f800000, v117
	v_cmp_gt_f32_e32 vcc, s8, v117
	s_nop 1
	v_cndmask_b32_e32 v117, v117, v128, vcc
	v_sqrt_f32_e32 v128, v117
	s_nop 0
	v_add_u32_e32 v138, -1, v128
	v_fma_f32 v140, -v138, v128, v117
	v_cmp_ge_f32_e64 s[0:1], 0, v140
	v_add_u32_e32 v140, 1, v128
	s_nop 0
	v_cndmask_b32_e64 v138, v128, v138, s[0:1]
	v_fma_f32 v128, -v140, v128, v117
	v_cmp_lt_f32_e64 s[0:1], 0, v128
	s_nop 1
	v_cndmask_b32_e64 v128, v138, v140, s[0:1]
	v_mul_f32_e32 v138, 0x37800000, v128
	v_cndmask_b32_e32 v128, v128, v138, vcc
	v_cmp_class_f32_e32 vcc, v117, v52
	v_mov_b32_e32 v140, v162
	s_nop 0
	v_cndmask_b32_e32 v117, v128, v117, vcc
	v_div_scale_f32 v128, s[0:1], v117, v117, 1.0
	v_rcp_f32_e32 v138, v128
	v_mov_b32_dpp v140, v124 quad_perm:[2,3,0,1] row_mask:0xf bank_mask:0xf
	v_fma_f32 v141, -v128, v138, 1.0
	v_fmac_f32_e32 v138, v141, v138
	v_div_scale_f32 v141, vcc, 1.0, v117, 1.0
	v_mul_f32_e32 v143, v141, v138
	v_fma_f32 v145, -v128, v143, v141
	v_fmac_f32_e32 v143, v145, v138
	v_fma_f32 v128, -v128, v143, v141
	v_div_fmas_f32 v128, v128, v138, v143
	v_div_fixup_f32 v141, v128, v117, 1.0
	v_pk_add_f32 v[124:125], v[124:125], v[140:141]
	v_pk_mul_f32 v[132:133], v[132:133], v[140:141]
	v_mul_f32_e32 v175, v115, v141
	v_mov_b32_e32 v125, v133
	v_mov_b32_e32 v132, v124
	v_mov_b32_e32 v133, v26
	v_pk_mul_f32 v[132:133], v[132:133], v[174:175]
	v_mul_f32_e32 v151, v129, v141
	v_add_f32_e32 v115, v30, v133
	v_mov_b32_e32 v128, v124
	v_mov_b32_e32 v129, v27
	v_add_f32_e32 v115, v132, v115
	v_pk_mul_f32 v[128:129], v[128:129], v[150:151]
	v_mul_f32_e32 v132, v115, v199
	v_add_f32_e32 v115, v31, v129
	v_add_f32_e32 v115, v128, v115
	v_mul_f32_e32 v155, v119, v141
	v_mov_b32_e32 v128, v124
	v_mov_b32_e32 v129, v28
; #define GAS __attribute__((address_space(1)))
; __device__ __forceinline__ void p5_post(Frame& F0, const In& I) {
;     ...
;         const float rstd = 1.f / sqrtf(s2 * (1.f / 64.f) + GN_EPS);
;         float o[16];
; #pragma unroll
;         for (int e = 0; e < 16; ++e) o[e] = (y[e] * rstd * p_lw[e] + p_lb[e] + bs * vv[e]) * gg[e];
;         { unsigned w8[4];
; #pragma unroll
;           for (int q = 0; q < 4; ++q) { int t8 = __builtin_amdgcn_cvt_pk_fp8_f32(o[4 * q] * ACT8_SCALE, o[4 * q + 1] * ACT8_SCALE, 0, false); t8 = __builtin_amdgcn_cvt_pk_fp8_f32(o[4 * q + 2] * ACT8_SCALE, o[4 * q + 3] * ACT8_SCALE, t8, true); w8[q] = (unsigned)t8; }
;           *(GAS v4u*)((unsigned char*)YB + (size_t)tok * RW + c0) = (v4u){w8[0], w8[1], w8[2], w8[3]}; }
	v_pk_mul_f32 v[128:129], v[128:129], v[154:155]
	v_mul_f32_e32 v133, v115, v200
	v_add_f32_e32 v115, v32, v129
	v_add_f32_e32 v115, v128, v115
	v_mul_f32_e32 v147, v121, v141
	v_mov_b32_e32 v128, v124
	v_mov_b32_e32 v129, v29
	v_pk_mul_f32 v[128:129], v[128:129], v[146:147]
	v_mul_f32_e32 v138, v115, v202
	v_add_f32_e32 v115, v33, v129
	v_add_f32_e32 v115, v128, v115
	v_mul_f32_e32 v149, v123, v141
	v_mov_b32_e32 v128, v124
	v_mov_b32_e32 v129, v34
	v_pk_mul_f32 v[128:129], v[128:129], v[148:149]
	v_mul_f32_e32 v140, v115, v203
	v_add_f32_e32 v115, v38, v129
	v_add_f32_e32 v115, v128, v115
	v_mul_f32_e32 v143, v127, v141
	v_mov_b32_e32 v128, v124
	v_mov_b32_e32 v129, v35
	v_pk_mul_f32 v[128:129], v[128:129], v[142:143]
	v_mul_f32_e32 v146, v115, v208
	v_add_f32_e32 v115, v39, v129
	v_add_f32_e32 v115, v128, v115
	v_mul_f32_e32 v145, v135, v141
	v_mov_b32_e32 v128, v124
	v_mov_b32_e32 v129, v36
	v_pk_mul_f32 v[128:129], v[128:129], v[144:145]
	v_mul_f32_e32 v142, v115, v209
	v_add_f32_e32 v115, v40, v129
	v_add_f32_e32 v115, v128, v115
	v_mul_f32_e32 v135, v137, v141
	v_mov_b32_e32 v128, v124
	v_mov_b32_e32 v129, v37
	v_pk_mul_f32 v[128:129], v[128:129], v[134:135]
	v_mul_f32_e32 v143, v115, v211
	v_add_f32_e32 v115, v41, v129
	v_add_f32_e32 v115, v128, v115
	v_mul_f32_e32 v137, v152, v141
	v_mov_b32_e32 v128, v124
	v_mov_b32_e32 v129, v42
	v_pk_mul_f32 v[128:129], v[128:129], v[136:137]
	v_mul_f32_e32 v134, v115, v212
	v_add_f32_e32 v115, v46, v129
	v_add_f32_e32 v115, v128, v115
	v_mul_f32_e32 v127, v153, v141
	v_mov_b32_e32 v128, v124
	v_mov_b32_e32 v129, v43
	v_pk_mul_f32 v[126:127], v[128:129], v[126:127]
	v_mul_f32_e32 v135, v115, v219
	v_add_f32_e32 v115, v47, v127
	v_add_f32_e32 v115, v126, v115
	v_mul_f32_e32 v123, v156, v141
	v_mov_b32_e32 v126, v124
	v_mov_b32_e32 v127, v44
	v_pk_mul_f32 v[122:123], v[126:127], v[122:123]
	v_mul_f32_e32 v128, v115, v220
	v_add_f32_e32 v115, v48, v123
	v_add_f32_e32 v115, v122, v115
	v_mul_f32_e32 v126, v115, v223
	v_mul_f32_e32 v115, v130, v141
	v_mov_b32_e32 v122, v124
	v_mov_b32_e32 v123, v45
	v_pk_mul_f32 v[114:115], v[122:123], v[114:115]
	v_mul_f32_e32 v121, v131, v141
	v_add_f32_e32 v115, v49, v115
	v_add_f32_e32 v114, v114, v115
	v_mul_f32_e32 v122, v114, v224
	v_mov_b32_e32 v114, v124
	v_mov_b32_e32 v115, v50
	v_pk_mul_f32 v[114:115], v[114:115], v[120:121]
	v_mul_f32_e32 v117, v139, v141
	v_add_f32_e32 v115, v54, v115
	v_add_f32_e32 v114, v114, v115
	v_mul_f32_e32 v120, v114, v225
	v_mov_b32_e32 v114, v124
	v_mov_b32_e32 v115, v51
	v_pk_mul_f32 v[114:115], v[114:115], v[116:117]
	v_mul_f32_e32 v119, v157, v141
	v_add_f32_e32 v115, v55, v115
	v_add_f32_e32 v114, v114, v115
	v_mul_f32_e32 v117, v114, v226
	v_pk_mul_f32 v[114:115], v[124:125], v[168:169]
	v_mov_b32_e32 v125, v53
	v_add_f32_e32 v115, v56, v115
	v_add_f32_e32 v114, v114, v115
	v_mul_f32_e32 v121, v114, v227
	v_pk_mul_f32 v[114:115], v[124:125], v[118:119]
	v_mul_f32_e32 v116, 0x41800000, v133
	v_add_f32_e32 v115, v57, v115
	v_add_f32_e32 v114, v114, v115
	v_mul_f32_e32 v118, v114, v228
	v_mul_f32_e32 v115, 0x41800000, v132
	v_mov_b32_e32 v114, v162
	v_cvt_pk_fp8_f32 v114, v115, v116
	v_mul_f32_e32 v123, 0x41800000, v146
	v_mul_f32_e32 v124, 0x41800000, v142
	v_mov_b32_e32 v115, v162
	v_cvt_pk_fp8_f32 v115, v123, v124
	v_mul_f32_e32 v116, 0x41800000, v138
	v_mul_f32_e32 v119, 0x41800000, v140
	v_cvt_pk_fp8_f32 v114, v116, v119 op_sel:[0,0,1]
	v_mul_f32_e32 v116, 0x41800000, v143
	v_mul_f32_e32 v119, 0x41800000, v134
	v_cvt_pk_fp8_f32 v115, v116, v119 op_sel:[0,0,1]
	v_mul_f32_e32 v119, 0x41800000, v135
	v_mul_f32_e32 v123, 0x41800000, v128
	v_mov_b32_e32 v116, v162
	v_cvt_pk_fp8_f32 v116, v119, v123
	v_mul_f32_e32 v120, 0x41800000, v120
	v_mul_f32_e32 v123, 0x41800000, v117
	v_mov_b32_e32 v117, v162
	v_cvt_pk_fp8_f32 v117, v120, v123
	v_mul_f32_e32 v119, 0x41800000, v126
	v_mul_f32_e32 v122, 0x41800000, v122
	v_cvt_pk_fp8_f32 v116, v119, v122 op_sel:[0,0,1]
	v_mul_f32_e32 v119, 0x41800000, v121
	v_mul_f32_e32 v118, 0x41800000, v118
	v_cvt_pk_fp8_f32 v117, v119, v118 op_sel:[0,0,1]
	v_lshl_add_u64 v[118:119], s[96:97], 0, v[166:167]
	s_waitcnt vmcnt(0)
	v_mov_b64_e32 v[160:161], v[108:109]
	v_mov_b64_e32 v[158:159], v[106:107]
	v_mov_b64_e32 v[136:137], v[68:69]
	v_mov_b64_e32 v[144:145], v[76:77]
	global_store_dwordx4 v[118:119], v[114:117], off
	v_mov_b64_e32 v[120:121], v[80:81]
	v_mov_b64_e32 v[148:149], v[84:85]
	v_mov_b64_e32 v[116:117], v[72:73]
	v_mov_b64_e32 v[124:125], v[88:89]
	v_mov_b64_e32 v[152:153], v[92:93]
	v_mov_b64_e32 v[128:129], v[96:97]
	v_mov_b64_e32 v[156:157], v[100:101]
	v_mov_b64_e32 v[132:133], v[104:105]
	v_mov_b64_e32 v[140:141], v[112:113]
	v_lshl_add_u64 v[166:167], v[166:167], 0, s[6:7]
	s_andn2_b64 vcc, exec, s[24:25]
	v_mov_b64_e32 v[134:135], v[66:67]
	v_mov_b64_e32 v[114:115], v[70:71]
	v_mov_b64_e32 v[142:143], v[74:75]
	v_mov_b64_e32 v[118:119], v[78:79]
	v_mov_b64_e32 v[146:147], v[82:83]
	v_mov_b64_e32 v[122:123], v[86:87]
	v_mov_b64_e32 v[150:151], v[90:91]
	v_mov_b64_e32 v[126:127], v[94:95]
	v_mov_b64_e32 v[154:155], v[98:99]
	v_mov_b64_e32 v[130:131], v[102:103]
	v_mov_b64_e32 v[138:139], v[110:111]
	s_cbranch_vccz .LBB0_1216
